# baseline (speedup 1.0000x reference)
.LBB3_3:
	s_lshl_b32 s3, s2, 2
	s_and_b32 s3, s3, 28
	s_bfe_u32 s2, s2, 0x20003
	s_load_dwordx2 s[10:11], s[0:1], 0x8
	s_load_dwordx2 s[12:13], s[0:1], 0x20
	s_or_b32 s2, s3, s2
	s_lshl_b32 s2, s2, 2
	s_or_b32 s6, s5, s2
	s_lshl_b32 s2, s6, 16
	s_waitcnt lgkmcnt(0)
	s_add_u32 s2, s10, s2
	s_addc_u32 s3, s11, 0
	v_lshl_add_u64 v[168:169], s[2:3], 0, v[134:135]
	s_movk_i32 s7, 0x1000
	v_add_co_u32_e32 v6, vcc, s7, v168
	s_movk_i32 s7, 0x2000
	s_nop 0
	v_addc_co_u32_e32 v7, vcc, 0, v169, vcc
	v_add_co_u32_e32 v8, vcc, s7, v168
	global_load_dwordx4 v[90:93], v134, s[2:3] offset:1024
	global_load_dwordx4 v[102:105], v134, s[2:3] offset:2048
	v_addc_co_u32_e32 v9, vcc, 0, v169, vcc
	global_load_dwordx4 v[106:109], v134, s[2:3] offset:3072
	global_load_dwordx4 v[94:97], v[8:9], off offset:-4096
	global_load_dwordx4 v[98:101], v[6:7], off offset:1024
	global_load_dwordx4 v[86:89], v[6:7], off offset:2048
	global_load_dwordx4 v[2:5], v134, s[2:3]
	global_load_dwordx4 v[82:85], v[6:7], off offset:3072
	global_load_dwordx4 v[78:81], v[8:9], off
	global_load_dwordx4 v[74:77], v[8:9], off offset:1024
	global_load_dwordx4 v[70:73], v[8:9], off offset:2048
	global_load_dwordx4 v[66:69], v[8:9], off offset:3072
	s_barrier
	ds_read_b128 v[6:9], v134
	ds_read_b128 v[10:13], v134 offset:4096
	ds_read_b128 v[14:17], v134 offset:8192
	ds_read_b128 v[110:113], v134 offset:12288
	s_load_dwordx2 s[2:3], s[0:1], 0x40
	s_lshl_b32 s7, s6, 6
	v_and_b32_e32 v1, 31, v0
	s_lshl_b32 s9, s4, 3
	v_lshrrev_b32_e32 v18, 2, v0
	s_add_i32 s10, s9, s7
	v_and_b32_e32 v18, 8, v18
	v_mov_b32_e32 v19, v135
	s_ashr_i32 s11, s10, 31
	v_lshl_add_u64 v[18:19], s[12:13], 0, v[18:19]
	s_lshl_b64 s[12:13], s[10:11], 10
	v_lshlrev_b32_e32 v1, 4, v1
	v_or_b32_e32 v20, s12, v1
	s_or_b32 s12, s10, 1
	v_mov_b32_e32 v21, s13
	s_ashr_i32 s13, s12, 31
	s_lshl_b64 s[12:13], s[12:13], 10
	v_or_b32_e32 v22, s12, v1
	s_or_b32 s12, s10, 2
	v_mov_b32_e32 v23, s13
	s_ashr_i32 s13, s12, 31
	v_lshl_add_u64 v[20:21], v[18:19], 0, v[20:21]
	s_lshl_b64 s[12:13], s[12:13], 10
	v_lshl_add_u64 v[22:23], v[18:19], 0, v[22:23]
	global_load_dwordx2 v[166:167], v[20:21], off
	global_load_dwordx2 v[164:165], v[20:21], off offset:512
	global_load_dwordx2 v[162:163], v[22:23], off
	global_load_dwordx2 v[160:161], v[22:23], off offset:512
	v_or_b32_e32 v20, s12, v1
	s_or_b32 s12, s10, 3
	v_mov_b32_e32 v21, s13
	s_ashr_i32 s13, s12, 31
	s_lshl_b64 s[12:13], s[12:13], 10
	v_or_b32_e32 v22, s12, v1
	s_or_b32 s12, s10, 4
	v_mov_b32_e32 v23, s13
	s_ashr_i32 s13, s12, 31
	v_lshl_add_u64 v[20:21], v[18:19], 0, v[20:21]
	s_lshl_b64 s[12:13], s[12:13], 10
	v_lshl_add_u64 v[22:23], v[18:19], 0, v[22:23]
	global_load_dwordx2 v[158:159], v[20:21], off
	global_load_dwordx2 v[156:157], v[20:21], off offset:512
	global_load_dwordx2 v[154:155], v[22:23], off
	global_load_dwordx2 v[152:153], v[22:23], off offset:512
	v_or_b32_e32 v20, s12, v1
	s_or_b32 s12, s10, 5
	v_mov_b32_e32 v21, s13
	s_ashr_i32 s13, s12, 31
	s_lshl_b64 s[12:13], s[12:13], 10
	v_or_b32_e32 v22, s12, v1
	s_or_b32 s12, s10, 6
	v_mov_b32_e32 v23, s13
	s_ashr_i32 s13, s12, 31
	s_or_b32 s10, s10, 7
	v_lshl_add_u64 v[20:21], v[18:19], 0, v[20:21]
	s_lshl_b64 s[12:13], s[12:13], 10
	s_ashr_i32 s11, s10, 31
	v_lshl_add_u64 v[22:23], v[18:19], 0, v[22:23]
	global_load_dwordx2 v[150:151], v[20:21], off
	global_load_dwordx2 v[148:149], v[20:21], off offset:512
	global_load_dwordx2 v[146:147], v[22:23], off
	global_load_dwordx2 v[144:145], v[22:23], off offset:512
	v_or_b32_e32 v20, s12, v1
	v_mov_b32_e32 v21, s13
	s_lshl_b64 s[10:11], s[10:11], 10
	v_lshl_add_u64 v[20:21], v[18:19], 0, v[20:21]
	v_or_b32_e32 v22, s10, v1
	v_mov_b32_e32 v23, s11
	v_lshl_add_u64 v[18:19], v[18:19], 0, v[22:23]
	global_load_dwordx2 v[142:143], v[20:21], off
	global_load_dwordx2 v[140:141], v[20:21], off offset:512
	global_load_dwordx2 v[138:139], v[18:19], off
	global_load_dwordx2 v[136:137], v[18:19], off offset:512
	s_lshl_b32 s7, s4, 7
	ds_read_b128 v[118:121], v134 offset:1024
	s_waitcnt vmcnt(21) lgkmcnt(0)
	v_mfma_f32_32x32x16_f16 v[50:65], v[6:9], v[2:5], 0
	s_movk_i32 s9, 0x4000
	v_add_co_u32_e32 v178, vcc, s9, v168
	ds_read_b128 v[122:125], v134 offset:5120
	s_nop 0
	v_addc_co_u32_e32 v179, vcc, 0, v169, vcc
	global_load_dwordx4 v[114:117], v[178:179], off offset:-4096
	s_movk_i32 s9, 0x3000
	v_add_co_u32_e32 v180, vcc, s9, v168
	v_mfma_f32_32x32x16_f16 v[34:49], v[10:13], v[2:5], 0
	s_nop 0
	v_addc_co_u32_e32 v181, vcc, 0, v169, vcc
	ds_read_b128 v[126:129], v134 offset:9216
	v_mfma_f32_32x32x16_f16 v[18:33], v[14:17], v[2:5], 0
	ds_read_b128 v[130:133], v134 offset:13312
	v_mfma_f32_32x32x16_f16 v[2:17], v[110:113], v[2:5], 0
	ds_read_b128 v[110:113], v134 offset:2048
	v_mfma_f32_32x32x16_f16 v[50:65], v[118:121], v[90:93], v[50:65]
	global_load_dwordx4 v[118:121], v[180:181], off offset:1024
	ds_read_b128 v[170:173], v134 offset:6144
	s_waitcnt lgkmcnt(4)
	v_mfma_f32_32x32x16_f16 v[34:49], v[122:125], v[90:93], v[34:49]
	ds_read_b128 v[174:177], v134 offset:10240
	s_waitcnt lgkmcnt(4)
	v_mfma_f32_32x32x16_f16 v[18:33], v[126:129], v[90:93], v[18:33]
	ds_read_b128 v[126:129], v134 offset:14336
	s_waitcnt lgkmcnt(4)
	v_mfma_f32_32x32x16_f16 v[2:17], v[130:133], v[90:93], v[2:17]
	ds_read_b128 v[90:93], v134 offset:3072
	s_waitcnt lgkmcnt(4)
	v_mfma_f32_32x32x16_f16 v[50:65], v[110:113], v[102:105], v[50:65]
	global_load_dwordx4 v[122:125], v[180:181], off offset:2048
	ds_read_b128 v[110:113], v134 offset:7168
	s_waitcnt lgkmcnt(4)
	v_mfma_f32_32x32x16_f16 v[34:49], v[170:173], v[102:105], v[34:49]
	ds_read_b128 v[130:133], v134 offset:11264
	s_waitcnt lgkmcnt(4)
	v_mfma_f32_32x32x16_f16 v[18:33], v[174:177], v[102:105], v[18:33]
	ds_read_b128 v[170:173], v134 offset:15360
	s_waitcnt lgkmcnt(4)
	v_mfma_f32_32x32x16_f16 v[2:17], v[126:129], v[102:105], v[2:17]
	global_load_dwordx4 v[102:105], v[180:181], off offset:3072
	s_waitcnt lgkmcnt(3)
	v_mfma_f32_32x32x16_f16 v[50:65], v[90:93], v[106:109], v[50:65]
	s_waitcnt lgkmcnt(0)
	s_barrier
	ds_read_b128 v[90:93], v134 offset:16384
	ds_read_b128 v[126:129], v134 offset:20480
	v_mfma_f32_32x32x16_f16 v[34:49], v[110:113], v[106:109], v[34:49]
	ds_read_b128 v[110:113], v134 offset:24576
	v_mfma_f32_32x32x16_f16 v[18:33], v[130:133], v[106:109], v[18:33]
	ds_read_b128 v[130:133], v134 offset:28672
	v_mfma_f32_32x32x16_f16 v[2:17], v[170:173], v[106:109], v[2:17]
	ds_read_b128 v[106:109], v134 offset:17408
	s_waitcnt lgkmcnt(4)
	v_mfma_f32_32x32x16_f16 v[50:65], v[90:93], v[94:97], v[50:65]
	global_load_dwordx4 v[90:93], v[178:179], off
	ds_read_b128 v[170:173], v134 offset:21504
	s_waitcnt lgkmcnt(4)
	v_mfma_f32_32x32x16_f16 v[34:49], v[126:129], v[94:97], v[34:49]
	ds_read_b128 v[126:129], v134 offset:25600
	s_waitcnt lgkmcnt(4)
	v_mfma_f32_32x32x16_f16 v[18:33], v[110:113], v[94:97], v[18:33]
	ds_read_b128 v[110:113], v134 offset:29696
	s_waitcnt lgkmcnt(4)
	v_mfma_f32_32x32x16_f16 v[2:17], v[130:133], v[94:97], v[2:17]
	ds_read_b128 v[130:133], v134 offset:18432
	s_waitcnt lgkmcnt(4)
	v_mfma_f32_32x32x16_f16 v[50:65], v[106:109], v[98:101], v[50:65]
	global_load_dwordx4 v[94:97], v[178:179], off offset:1024
	ds_read_b128 v[106:109], v134 offset:22528
	s_waitcnt lgkmcnt(4)
	v_mfma_f32_32x32x16_f16 v[34:49], v[170:173], v[98:101], v[34:49]
	ds_read_b128 v[170:173], v134 offset:26624
	s_waitcnt lgkmcnt(4)
	v_mfma_f32_32x32x16_f16 v[18:33], v[126:129], v[98:101], v[18:33]
	ds_read_b128 v[126:129], v134 offset:30720
	s_waitcnt lgkmcnt(4)
	v_mfma_f32_32x32x16_f16 v[2:17], v[110:113], v[98:101], v[2:17]
	ds_read_b128 v[110:113], v134 offset:19456
	s_waitcnt lgkmcnt(4)
	v_mfma_f32_32x32x16_f16 v[50:65], v[130:133], v[86:89], v[50:65]
	global_load_dwordx4 v[98:101], v[178:179], off offset:2048
	ds_read_b128 v[130:133], v134 offset:23552
	s_waitcnt lgkmcnt(4)
	v_mfma_f32_32x32x16_f16 v[34:49], v[106:109], v[86:89], v[34:49]
	ds_read_b128 v[106:109], v134 offset:27648
	s_waitcnt lgkmcnt(4)
	v_mfma_f32_32x32x16_f16 v[18:33], v[170:173], v[86:89], v[18:33]
	ds_read_b128 v[170:173], v134 offset:31744
	s_waitcnt lgkmcnt(4)
	v_mfma_f32_32x32x16_f16 v[2:17], v[126:129], v[86:89], v[2:17]
	global_load_dwordx4 v[86:89], v[178:179], off offset:3072
	s_waitcnt vmcnt(28) lgkmcnt(3)
	v_mfma_f32_32x32x16_f16 v[50:65], v[110:113], v[82:85], v[50:65]
	s_waitcnt lgkmcnt(0)
	s_barrier
	ds_read_b128 v[110:113], v134
	ds_read_b128 v[126:129], v134 offset:4096
	v_mfma_f32_32x32x16_f16 v[34:49], v[130:133], v[82:85], v[34:49]
	ds_read_b128 v[130:133], v134 offset:8192
	v_mfma_f32_32x32x16_f16 v[18:33], v[106:109], v[82:85], v[18:33]
	ds_read_b128 v[106:109], v134 offset:12288
	v_mfma_f32_32x32x16_f16 v[2:17], v[170:173], v[82:85], v[2:17]
	ds_read_b128 v[82:85], v134 offset:1024
	s_waitcnt vmcnt(27) lgkmcnt(4)
	v_mfma_f32_32x32x16_f16 v[50:65], v[110:113], v[78:81], v[50:65]
	s_movk_i32 s9, 0x6000
	v_add_co_u32_e32 v178, vcc, s9, v168
	ds_read_b128 v[170:173], v134 offset:5120
	s_nop 0
	v_addc_co_u32_e32 v179, vcc, 0, v169, vcc
	global_load_dwordx4 v[110:113], v[178:179], off offset:-4096
	s_movk_i32 s9, 0x5000
	v_add_co_u32_e32 v180, vcc, s9, v168
	s_waitcnt lgkmcnt(4)
	v_mfma_f32_32x32x16_f16 v[34:49], v[126:129], v[78:81], v[34:49]
	v_addc_co_u32_e32 v181, vcc, 0, v169, vcc
	ds_read_b128 v[174:177], v134 offset:9216
	s_waitcnt lgkmcnt(4)
	v_mfma_f32_32x32x16_f16 v[18:33], v[130:133], v[78:81], v[18:33]
	ds_read_b128 v[130:133], v134 offset:13312
	s_waitcnt lgkmcnt(4)
	v_mfma_f32_32x32x16_f16 v[2:17], v[106:109], v[78:81], v[2:17]
	ds_read_b128 v[78:81], v134 offset:2048
	s_waitcnt vmcnt(27) lgkmcnt(4)
	v_mfma_f32_32x32x16_f16 v[50:65], v[82:85], v[74:77], v[50:65]
	global_load_dwordx4 v[126:129], v[180:181], off offset:1024
	ds_read_b128 v[82:85], v134 offset:6144
	s_waitcnt lgkmcnt(4)
	v_mfma_f32_32x32x16_f16 v[34:49], v[170:173], v[74:77], v[34:49]
	ds_read_b128 v[106:109], v134 offset:10240
	s_waitcnt lgkmcnt(4)
	v_mfma_f32_32x32x16_f16 v[18:33], v[174:177], v[74:77], v[18:33]
	ds_read_b128 v[170:173], v134 offset:14336
	s_waitcnt lgkmcnt(4)
	v_mfma_f32_32x32x16_f16 v[2:17], v[130:133], v[74:77], v[2:17]
	ds_read_b128 v[74:77], v134 offset:3072
	s_waitcnt vmcnt(27) lgkmcnt(4)
	v_mfma_f32_32x32x16_f16 v[50:65], v[78:81], v[70:73], v[50:65]
	global_load_dwordx4 v[130:133], v[180:181], off offset:2048
	ds_read_b128 v[78:81], v134 offset:7168
	s_waitcnt lgkmcnt(4)
	v_mfma_f32_32x32x16_f16 v[34:49], v[82:85], v[70:73], v[34:49]
	ds_read_b128 v[82:85], v134 offset:11264
	s_waitcnt lgkmcnt(4)
	v_mfma_f32_32x32x16_f16 v[18:33], v[106:109], v[70:73], v[18:33]
	ds_read_b128 v[174:177], v134 offset:15360
	s_waitcnt lgkmcnt(4)
	v_mfma_f32_32x32x16_f16 v[2:17], v[170:173], v[70:73], v[2:17]
	global_load_dwordx4 v[106:109], v[180:181], off offset:3072
	s_waitcnt vmcnt(28) lgkmcnt(3)
	v_mfma_f32_32x32x16_f16 v[50:65], v[74:77], v[66:69], v[50:65]
	s_waitcnt lgkmcnt(0)
	s_barrier
	ds_read_b128 v[70:73], v134 offset:16384
	ds_read_b128 v[170:173], v134 offset:20480
	v_mfma_f32_32x32x16_f16 v[34:49], v[78:81], v[66:69], v[34:49]
	ds_read_b128 v[78:81], v134 offset:24576
	v_mfma_f32_32x32x16_f16 v[18:33], v[82:85], v[66:69], v[18:33]
	ds_read_b128 v[82:85], v134 offset:28672
	v_mfma_f32_32x32x16_f16 v[2:17], v[174:177], v[66:69], v[2:17]
	ds_read_b128 v[66:69], v134 offset:17408
	s_waitcnt vmcnt(11) lgkmcnt(4)
	v_mfma_f32_32x32x16_f16 v[50:65], v[70:73], v[114:117], v[50:65]
	global_load_dwordx4 v[74:77], v[178:179], off
	ds_read_b128 v[70:73], v134 offset:21504
	s_waitcnt lgkmcnt(4)
	v_mfma_f32_32x32x16_f16 v[34:49], v[170:173], v[114:117], v[34:49]
	ds_read_b128 v[170:173], v134 offset:25600
	s_waitcnt lgkmcnt(4)
	v_mfma_f32_32x32x16_f16 v[18:33], v[78:81], v[114:117], v[18:33]
	ds_read_b128 v[174:177], v134 offset:29696
	s_waitcnt lgkmcnt(4)
	v_mfma_f32_32x32x16_f16 v[2:17], v[82:85], v[114:117], v[2:17]
	ds_read_b128 v[82:85], v134 offset:18432
	s_waitcnt vmcnt(11) lgkmcnt(4)
	v_mfma_f32_32x32x16_f16 v[50:65], v[66:69], v[118:121], v[50:65]
	global_load_dwordx4 v[78:81], v[178:179], off offset:1024
	ds_read_b128 v[66:69], v134 offset:22528
	s_waitcnt lgkmcnt(4)
	v_mfma_f32_32x32x16_f16 v[34:49], v[70:73], v[118:121], v[34:49]
	ds_read_b128 v[70:73], v134 offset:26624
	s_waitcnt lgkmcnt(4)
	v_mfma_f32_32x32x16_f16 v[18:33], v[170:173], v[118:121], v[18:33]
	ds_read_b128 v[114:117], v134 offset:30720
	s_waitcnt lgkmcnt(4)
	v_mfma_f32_32x32x16_f16 v[2:17], v[174:177], v[118:121], v[2:17]
	ds_read_b128 v[118:121], v134 offset:19456
	s_waitcnt vmcnt(11) lgkmcnt(4)
	v_mfma_f32_32x32x16_f16 v[50:65], v[82:85], v[122:125], v[50:65]
	global_load_dwordx4 v[82:85], v[178:179], off offset:2048
	ds_read_b128 v[170:173], v134 offset:23552
	s_waitcnt lgkmcnt(4)
	v_mfma_f32_32x32x16_f16 v[34:49], v[66:69], v[122:125], v[34:49]
	ds_read_b128 v[174:177], v134 offset:27648
	s_waitcnt lgkmcnt(4)
	v_mfma_f32_32x32x16_f16 v[18:33], v[70:73], v[122:125], v[18:33]
	ds_read_b128 v[70:73], v134 offset:31744
	s_waitcnt lgkmcnt(4)
	v_mfma_f32_32x32x16_f16 v[2:17], v[114:117], v[122:125], v[2:17]
	global_load_dwordx4 v[66:69], v[178:179], off offset:3072
	s_waitcnt vmcnt(12) lgkmcnt(3)
	v_mfma_f32_32x32x16_f16 v[50:65], v[118:121], v[102:105], v[50:65]
	s_waitcnt lgkmcnt(0)
	s_barrier
	ds_read_b128 v[114:117], v134
	ds_read_b128 v[118:121], v134 offset:4096
	v_mfma_f32_32x32x16_f16 v[34:49], v[170:173], v[102:105], v[34:49]
	ds_read_b128 v[122:125], v134 offset:8192
	v_mfma_f32_32x32x16_f16 v[18:33], v[174:177], v[102:105], v[18:33]
	ds_read_b128 v[170:173], v134 offset:12288
	v_mfma_f32_32x32x16_f16 v[2:17], v[70:73], v[102:105], v[2:17]
	ds_read_b128 v[70:73], v134 offset:1024
	s_waitcnt vmcnt(11) lgkmcnt(4)
	v_mfma_f32_32x32x16_f16 v[50:65], v[114:117], v[90:93], v[50:65]
	s_mov_b32 s9, 0x8000
	v_add_co_u32_e32 v178, vcc, s9, v168
	ds_read_b128 v[102:105], v134 offset:5120
	s_nop 0
	v_addc_co_u32_e32 v179, vcc, 0, v169, vcc
	global_load_dwordx4 v[114:117], v[178:179], off offset:-4096
	s_movk_i32 s9, 0x7000
	v_add_co_u32_e32 v180, vcc, s9, v168
	s_waitcnt lgkmcnt(4)
	v_mfma_f32_32x32x16_f16 v[34:49], v[118:121], v[90:93], v[34:49]
	v_addc_co_u32_e32 v181, vcc, 0, v169, vcc
	ds_read_b128 v[174:177], v134 offset:9216
	s_waitcnt lgkmcnt(4)
	v_mfma_f32_32x32x16_f16 v[18:33], v[122:125], v[90:93], v[18:33]
	ds_read_b128 v[122:125], v134 offset:13312
	s_waitcnt lgkmcnt(4)
	v_mfma_f32_32x32x16_f16 v[2:17], v[170:173], v[90:93], v[2:17]
	ds_read_b128 v[90:93], v134 offset:2048
	s_waitcnt vmcnt(11) lgkmcnt(4)
	v_mfma_f32_32x32x16_f16 v[50:65], v[70:73], v[94:97], v[50:65]
	global_load_dwordx4 v[118:121], v[180:181], off offset:1024
	ds_read_b128 v[70:73], v134 offset:6144
	s_waitcnt lgkmcnt(4)
	v_mfma_f32_32x32x16_f16 v[34:49], v[102:105], v[94:97], v[34:49]
	ds_read_b128 v[102:105], v134 offset:10240
	s_waitcnt lgkmcnt(4)
	v_mfma_f32_32x32x16_f16 v[18:33], v[174:177], v[94:97], v[18:33]
	ds_read_b128 v[170:173], v134 offset:14336
	s_waitcnt lgkmcnt(4)
	v_mfma_f32_32x32x16_f16 v[2:17], v[122:125], v[94:97], v[2:17]
	ds_read_b128 v[94:97], v134 offset:3072
	s_waitcnt vmcnt(11) lgkmcnt(4)
	v_mfma_f32_32x32x16_f16 v[50:65], v[90:93], v[98:101], v[50:65]
	global_load_dwordx4 v[122:125], v[180:181], off offset:2048
	ds_read_b128 v[90:93], v134 offset:7168
	s_waitcnt lgkmcnt(4)
	v_mfma_f32_32x32x16_f16 v[34:49], v[70:73], v[98:101], v[34:49]
	ds_read_b128 v[70:73], v134 offset:11264
	s_waitcnt lgkmcnt(4)
	v_mfma_f32_32x32x16_f16 v[18:33], v[102:105], v[98:101], v[18:33]
	ds_read_b128 v[174:177], v134 offset:15360
	s_waitcnt lgkmcnt(4)
	v_mfma_f32_32x32x16_f16 v[2:17], v[170:173], v[98:101], v[2:17]
	global_load_dwordx4 v[102:105], v[180:181], off offset:3072
	s_waitcnt vmcnt(12) lgkmcnt(3)
	v_mfma_f32_32x32x16_f16 v[50:65], v[94:97], v[86:89], v[50:65]
	s_waitcnt lgkmcnt(0)
	s_barrier
	ds_read_b128 v[94:97], v134 offset:16384
	ds_read_b128 v[98:101], v134 offset:20480
	v_mfma_f32_32x32x16_f16 v[34:49], v[90:93], v[86:89], v[34:49]
	ds_read_b128 v[90:93], v134 offset:24576
	v_mfma_f32_32x32x16_f16 v[18:33], v[70:73], v[86:89], v[18:33]
	ds_read_b128 v[70:73], v134 offset:28672
	v_mfma_f32_32x32x16_f16 v[2:17], v[174:177], v[86:89], v[2:17]
	ds_read_b128 v[170:173], v134 offset:17408
	s_waitcnt vmcnt(11) lgkmcnt(4)
	v_mfma_f32_32x32x16_f16 v[50:65], v[94:97], v[110:113], v[50:65]
	global_load_dwordx4 v[86:89], v[178:179], off
	ds_read_b128 v[94:97], v134 offset:21504
	s_waitcnt lgkmcnt(4)
	v_mfma_f32_32x32x16_f16 v[34:49], v[98:101], v[110:113], v[34:49]
	ds_read_b128 v[98:101], v134 offset:25600
	s_waitcnt lgkmcnt(4)
	v_mfma_f32_32x32x16_f16 v[18:33], v[90:93], v[110:113], v[18:33]
	ds_read_b128 v[174:177], v134 offset:29696
	s_waitcnt lgkmcnt(4)
	v_mfma_f32_32x32x16_f16 v[2:17], v[70:73], v[110:113], v[2:17]
	ds_read_b128 v[70:73], v134 offset:18432
	s_waitcnt vmcnt(11) lgkmcnt(4)
	v_mfma_f32_32x32x16_f16 v[50:65], v[170:173], v[126:129], v[50:65]
	global_load_dwordx4 v[90:93], v[178:179], off offset:1024
	ds_read_b128 v[110:113], v134 offset:22528
	s_waitcnt lgkmcnt(4)
	v_mfma_f32_32x32x16_f16 v[34:49], v[94:97], v[126:129], v[34:49]
	ds_read_b128 v[170:173], v134 offset:26624
	s_waitcnt lgkmcnt(4)
	v_mfma_f32_32x32x16_f16 v[18:33], v[98:101], v[126:129], v[18:33]
	ds_read_b128 v[98:101], v134 offset:30720
	s_waitcnt lgkmcnt(4)
	v_mfma_f32_32x32x16_f16 v[2:17], v[174:177], v[126:129], v[2:17]
	ds_read_b128 v[126:129], v134 offset:19456
	s_waitcnt vmcnt(11) lgkmcnt(4)
	v_mfma_f32_32x32x16_f16 v[50:65], v[70:73], v[130:133], v[50:65]
	global_load_dwordx4 v[94:97], v[178:179], off offset:2048
	ds_read_b128 v[174:177], v134 offset:23552
	s_waitcnt lgkmcnt(4)
	v_mfma_f32_32x32x16_f16 v[34:49], v[110:113], v[130:133], v[34:49]
	ds_read_b128 v[110:113], v134 offset:27648
	s_waitcnt lgkmcnt(4)
	v_mfma_f32_32x32x16_f16 v[18:33], v[170:173], v[130:133], v[18:33]
	ds_read_b128 v[170:173], v134 offset:31744
	s_waitcnt lgkmcnt(4)
	v_mfma_f32_32x32x16_f16 v[2:17], v[98:101], v[130:133], v[2:17]
	global_load_dwordx4 v[70:73], v[178:179], off offset:3072
	s_waitcnt vmcnt(12) lgkmcnt(3)
	v_mfma_f32_32x32x16_f16 v[50:65], v[126:129], v[106:109], v[50:65]
	s_waitcnt lgkmcnt(0)
	s_barrier
	ds_read_b128 v[98:101], v134
	ds_read_b128 v[126:129], v134 offset:4096
	v_mfma_f32_32x32x16_f16 v[34:49], v[174:177], v[106:109], v[34:49]
	ds_read_b128 v[130:133], v134 offset:8192
	v_mfma_f32_32x32x16_f16 v[18:33], v[110:113], v[106:109], v[18:33]
	ds_read_b128 v[174:177], v134 offset:12288
	v_mfma_f32_32x32x16_f16 v[2:17], v[170:173], v[106:109], v[2:17]
	ds_read_b128 v[106:109], v134 offset:1024
	s_waitcnt vmcnt(11) lgkmcnt(4)
	v_mfma_f32_32x32x16_f16 v[50:65], v[98:101], v[74:77], v[50:65]
	s_mov_b32 s9, 0xa000
	v_add_co_u32_e32 v178, vcc, s9, v168
	ds_read_b128 v[98:101], v134 offset:5120
	s_nop 0
	v_addc_co_u32_e32 v179, vcc, 0, v169, vcc
	global_load_dwordx4 v[110:113], v[178:179], off offset:-4096
	s_mov_b32 s9, 0x9000
	v_add_co_u32_e32 v180, vcc, s9, v168
	s_waitcnt lgkmcnt(4)
	v_mfma_f32_32x32x16_f16 v[34:49], v[126:129], v[74:77], v[34:49]
	v_addc_co_u32_e32 v181, vcc, 0, v169, vcc
	ds_read_b128 v[170:173], v134 offset:9216
	s_waitcnt lgkmcnt(4)
	v_mfma_f32_32x32x16_f16 v[18:33], v[130:133], v[74:77], v[18:33]
	ds_read_b128 v[130:133], v134 offset:13312
	s_waitcnt lgkmcnt(4)
	v_mfma_f32_32x32x16_f16 v[2:17], v[174:177], v[74:77], v[2:17]
	ds_read_b128 v[74:77], v134 offset:2048
	s_waitcnt vmcnt(11) lgkmcnt(4)
	v_mfma_f32_32x32x16_f16 v[50:65], v[106:109], v[78:81], v[50:65]
	global_load_dwordx4 v[126:129], v[180:181], off offset:1024
	ds_read_b128 v[106:109], v134 offset:6144
	s_waitcnt lgkmcnt(4)
	v_mfma_f32_32x32x16_f16 v[34:49], v[98:101], v[78:81], v[34:49]
	ds_read_b128 v[98:101], v134 offset:10240
	s_waitcnt lgkmcnt(4)
	v_mfma_f32_32x32x16_f16 v[18:33], v[170:173], v[78:81], v[18:33]
	ds_read_b128 v[170:173], v134 offset:14336
	s_waitcnt lgkmcnt(4)
	v_mfma_f32_32x32x16_f16 v[2:17], v[130:133], v[78:81], v[2:17]
	ds_read_b128 v[78:81], v134 offset:3072
	s_waitcnt vmcnt(11) lgkmcnt(4)
	v_mfma_f32_32x32x16_f16 v[50:65], v[74:77], v[82:85], v[50:65]
	global_load_dwordx4 v[130:133], v[180:181], off offset:2048
	ds_read_b128 v[74:77], v134 offset:7168
	s_waitcnt lgkmcnt(4)
	v_mfma_f32_32x32x16_f16 v[34:49], v[106:109], v[82:85], v[34:49]
	ds_read_b128 v[174:177], v134 offset:11264
	s_waitcnt lgkmcnt(4)
	v_mfma_f32_32x32x16_f16 v[18:33], v[98:101], v[82:85], v[18:33]
	ds_read_b128 v[98:101], v134 offset:15360
	s_waitcnt lgkmcnt(4)
	v_mfma_f32_32x32x16_f16 v[2:17], v[170:173], v[82:85], v[2:17]
	global_load_dwordx4 v[106:109], v[180:181], off offset:3072
	s_waitcnt vmcnt(12) lgkmcnt(3)
	v_mfma_f32_32x32x16_f16 v[50:65], v[78:81], v[66:69], v[50:65]
	s_waitcnt lgkmcnt(0)
	s_barrier
	ds_read_b128 v[78:81], v134 offset:16384
	ds_read_b128 v[82:85], v134 offset:20480
	v_mfma_f32_32x32x16_f16 v[34:49], v[74:77], v[66:69], v[34:49]
	ds_read_b128 v[74:77], v134 offset:24576
	v_mfma_f32_32x32x16_f16 v[18:33], v[174:177], v[66:69], v[18:33]
	ds_read_b128 v[170:173], v134 offset:28672
	v_mfma_f32_32x32x16_f16 v[2:17], v[98:101], v[66:69], v[2:17]
	ds_read_b128 v[66:69], v134 offset:17408
	s_waitcnt vmcnt(11) lgkmcnt(4)
	v_mfma_f32_32x32x16_f16 v[50:65], v[78:81], v[114:117], v[50:65]
	global_load_dwordx4 v[78:81], v[178:179], off
	ds_read_b128 v[98:101], v134 offset:21504
	s_waitcnt lgkmcnt(4)
	v_mfma_f32_32x32x16_f16 v[34:49], v[82:85], v[114:117], v[34:49]
	ds_read_b128 v[174:177], v134 offset:25600
	s_waitcnt lgkmcnt(4)
	v_mfma_f32_32x32x16_f16 v[18:33], v[74:77], v[114:117], v[18:33]
	ds_read_b128 v[74:77], v134 offset:29696
	s_waitcnt lgkmcnt(4)
	v_mfma_f32_32x32x16_f16 v[2:17], v[170:173], v[114:117], v[2:17]
	ds_read_b128 v[114:117], v134 offset:18432
	s_waitcnt vmcnt(11) lgkmcnt(4)
	v_mfma_f32_32x32x16_f16 v[50:65], v[66:69], v[118:121], v[50:65]
	global_load_dwordx4 v[82:85], v[178:179], off offset:1024
	ds_read_b128 v[66:69], v134 offset:22528
	s_waitcnt lgkmcnt(4)
	v_mfma_f32_32x32x16_f16 v[34:49], v[98:101], v[118:121], v[34:49]
	ds_read_b128 v[170:173], v134 offset:26624
	s_waitcnt lgkmcnt(4)
	v_mfma_f32_32x32x16_f16 v[18:33], v[174:177], v[118:121], v[18:33]
	ds_read_b128 v[174:177], v134 offset:30720
	s_waitcnt lgkmcnt(4)
	v_mfma_f32_32x32x16_f16 v[2:17], v[74:77], v[118:121], v[2:17]
	ds_read_b128 v[118:121], v134 offset:19456
	s_waitcnt vmcnt(11) lgkmcnt(4)
	v_mfma_f32_32x32x16_f16 v[50:65], v[114:117], v[122:125], v[50:65]
	global_load_dwordx4 v[98:101], v[178:179], off offset:2048
	ds_read_b128 v[114:117], v134 offset:23552
	s_waitcnt lgkmcnt(4)
	v_mfma_f32_32x32x16_f16 v[34:49], v[66:69], v[122:125], v[34:49]
	ds_read_b128 v[66:69], v134 offset:27648
	s_waitcnt lgkmcnt(4)
	v_mfma_f32_32x32x16_f16 v[18:33], v[170:173], v[122:125], v[18:33]
	ds_read_b128 v[170:173], v134 offset:31744
	s_waitcnt lgkmcnt(4)
	v_mfma_f32_32x32x16_f16 v[2:17], v[174:177], v[122:125], v[2:17]
	global_load_dwordx4 v[74:77], v[178:179], off offset:3072
	s_waitcnt vmcnt(12) lgkmcnt(3)
	v_mfma_f32_32x32x16_f16 v[50:65], v[118:121], v[102:105], v[50:65]
	s_waitcnt lgkmcnt(0)
	s_barrier
	ds_read_b128 v[118:121], v134
	ds_read_b128 v[122:125], v134 offset:4096
	v_mfma_f32_32x32x16_f16 v[34:49], v[114:117], v[102:105], v[34:49]
	ds_read_b128 v[174:177], v134 offset:8192
	v_mfma_f32_32x32x16_f16 v[18:33], v[66:69], v[102:105], v[18:33]
	ds_read_b128 v[66:69], v134 offset:12288
	v_mfma_f32_32x32x16_f16 v[2:17], v[170:173], v[102:105], v[2:17]
	ds_read_b128 v[102:105], v134 offset:1024
	s_waitcnt vmcnt(11) lgkmcnt(4)
	v_mfma_f32_32x32x16_f16 v[50:65], v[118:121], v[86:89], v[50:65]
	s_mov_b32 s9, 0xc000
	v_add_co_u32_e32 v178, vcc, s9, v168
	s_waitcnt lgkmcnt(3)
	v_mfma_f32_32x32x16_f16 v[34:49], v[122:125], v[86:89], v[34:49]
	v_addc_co_u32_e32 v179, vcc, 0, v169, vcc
	global_load_dwordx4 v[114:117], v[178:179], off offset:-4096
	ds_read_b128 v[122:125], v134 offset:5120
	s_mov_b32 s9, 0xb000
	v_add_co_u32_e32 v180, vcc, s9, v168
	s_nop 1
	v_addc_co_u32_e32 v181, vcc, 0, v169, vcc
	ds_read_b128 v[170:173], v134 offset:9216
	s_waitcnt lgkmcnt(4)
	v_mfma_f32_32x32x16_f16 v[18:33], v[174:177], v[86:89], v[18:33]
	ds_read_b128 v[174:177], v134 offset:13312
	s_waitcnt lgkmcnt(4)
	v_mfma_f32_32x32x16_f16 v[2:17], v[66:69], v[86:89], v[2:17]
	ds_read_b128 v[66:69], v134 offset:2048
	s_waitcnt vmcnt(11) lgkmcnt(4)
	v_mfma_f32_32x32x16_f16 v[50:65], v[102:105], v[90:93], v[50:65]
	global_load_dwordx4 v[118:121], v[180:181], off offset:1024
	ds_read_b128 v[86:89], v134 offset:6144
	s_waitcnt lgkmcnt(4)
	v_mfma_f32_32x32x16_f16 v[34:49], v[122:125], v[90:93], v[34:49]
	ds_read_b128 v[102:105], v134 offset:10240
	s_waitcnt lgkmcnt(4)
	v_mfma_f32_32x32x16_f16 v[18:33], v[170:173], v[90:93], v[18:33]
	ds_read_b128 v[170:173], v134 offset:14336
	s_waitcnt lgkmcnt(4)
	v_mfma_f32_32x32x16_f16 v[2:17], v[174:177], v[90:93], v[2:17]
	ds_read_b128 v[90:93], v134 offset:3072
	s_waitcnt vmcnt(11) lgkmcnt(4)
	v_mfma_f32_32x32x16_f16 v[50:65], v[66:69], v[94:97], v[50:65]
	global_load_dwordx4 v[122:125], v[180:181], off offset:2048
	ds_read_b128 v[66:69], v134 offset:7168
	s_waitcnt lgkmcnt(4)
	v_mfma_f32_32x32x16_f16 v[34:49], v[86:89], v[94:97], v[34:49]
	ds_read_b128 v[86:89], v134 offset:11264
	s_waitcnt lgkmcnt(4)
	v_mfma_f32_32x32x16_f16 v[18:33], v[102:105], v[94:97], v[18:33]
	ds_read_b128 v[102:105], v134 offset:15360
	s_waitcnt lgkmcnt(4)
	v_mfma_f32_32x32x16_f16 v[2:17], v[170:173], v[94:97], v[2:17]
	global_load_dwordx4 v[94:97], v[180:181], off offset:3072
	s_waitcnt vmcnt(12) lgkmcnt(3)
	v_mfma_f32_32x32x16_f16 v[50:65], v[90:93], v[70:73], v[50:65]
	s_waitcnt lgkmcnt(0)
	s_barrier
	ds_read_b128 v[90:93], v134 offset:16384
	ds_read_b128 v[170:173], v134 offset:20480
	v_mfma_f32_32x32x16_f16 v[34:49], v[66:69], v[70:73], v[34:49]
	ds_read_b128 v[66:69], v134 offset:24576
	v_mfma_f32_32x32x16_f16 v[18:33], v[86:89], v[70:73], v[18:33]
	ds_read_b128 v[86:89], v134 offset:28672
	v_mfma_f32_32x32x16_f16 v[2:17], v[102:105], v[70:73], v[2:17]
	ds_read_b128 v[70:73], v134 offset:17408
	s_waitcnt vmcnt(11) lgkmcnt(4)
	v_mfma_f32_32x32x16_f16 v[50:65], v[90:93], v[110:113], v[50:65]
	global_load_dwordx4 v[102:105], v[178:179], off
	ds_read_b128 v[90:93], v134 offset:21504
	s_waitcnt lgkmcnt(4)
	v_mfma_f32_32x32x16_f16 v[34:49], v[170:173], v[110:113], v[34:49]
	ds_read_b128 v[170:173], v134 offset:25600
	s_waitcnt lgkmcnt(4)
	v_mfma_f32_32x32x16_f16 v[18:33], v[66:69], v[110:113], v[18:33]
	ds_read_b128 v[66:69], v134 offset:29696
	s_waitcnt lgkmcnt(4)
	v_mfma_f32_32x32x16_f16 v[2:17], v[86:89], v[110:113], v[2:17]
	ds_read_b128 v[110:113], v134 offset:18432
	s_waitcnt vmcnt(11) lgkmcnt(4)
	v_mfma_f32_32x32x16_f16 v[50:65], v[70:73], v[126:129], v[50:65]
	global_load_dwordx4 v[86:89], v[178:179], off offset:1024
	ds_read_b128 v[174:177], v134 offset:22528
	s_waitcnt lgkmcnt(4)
	v_mfma_f32_32x32x16_f16 v[34:49], v[90:93], v[126:129], v[34:49]
	ds_read_b128 v[90:93], v134 offset:26624
	s_waitcnt lgkmcnt(4)
	v_mfma_f32_32x32x16_f16 v[18:33], v[170:173], v[126:129], v[18:33]
	ds_read_b128 v[170:173], v134 offset:30720
	s_waitcnt lgkmcnt(4)
	v_mfma_f32_32x32x16_f16 v[2:17], v[66:69], v[126:129], v[2:17]
	ds_read_b128 v[126:129], v134 offset:19456
	s_waitcnt vmcnt(11) lgkmcnt(4)
	v_mfma_f32_32x32x16_f16 v[50:65], v[110:113], v[130:133], v[50:65]
	global_load_dwordx4 v[70:73], v[178:179], off offset:2048
	ds_read_b128 v[110:113], v134 offset:23552
	s_waitcnt lgkmcnt(4)
	v_mfma_f32_32x32x16_f16 v[34:49], v[174:177], v[130:133], v[34:49]
	ds_read_b128 v[174:177], v134 offset:27648
	s_waitcnt lgkmcnt(4)
	v_mfma_f32_32x32x16_f16 v[18:33], v[90:93], v[130:133], v[18:33]
	ds_read_b128 v[90:93], v134 offset:31744
	s_waitcnt lgkmcnt(4)
	v_mfma_f32_32x32x16_f16 v[2:17], v[170:173], v[130:133], v[2:17]
	global_load_dwordx4 v[66:69], v[178:179], off offset:3072
	s_waitcnt vmcnt(12) lgkmcnt(3)
	v_mfma_f32_32x32x16_f16 v[50:65], v[126:129], v[106:109], v[50:65]
	s_waitcnt lgkmcnt(0)
	s_barrier
	ds_read_b128 v[126:129], v134
	ds_read_b128 v[130:133], v134 offset:4096
	v_mfma_f32_32x32x16_f16 v[34:49], v[110:113], v[106:109], v[34:49]
	ds_read_b128 v[110:113], v134 offset:8192
	v_mfma_f32_32x32x16_f16 v[18:33], v[174:177], v[106:109], v[18:33]
	ds_read_b128 v[170:173], v134 offset:12288
	v_mfma_f32_32x32x16_f16 v[2:17], v[90:93], v[106:109], v[2:17]
	ds_read_b128 v[106:109], v134 offset:1024
	s_waitcnt vmcnt(11) lgkmcnt(4)
	v_mfma_f32_32x32x16_f16 v[50:65], v[126:129], v[78:81], v[50:65]
	s_mov_b32 s9, 0xe000
	v_add_co_u32_e32 v178, vcc, s9, v168
	ds_read_b128 v[126:129], v134 offset:5120
	s_nop 0
	v_addc_co_u32_e32 v179, vcc, 0, v169, vcc
	global_load_dwordx4 v[90:93], v[178:179], off offset:-4096
	s_mov_b32 s9, 0xd000
	v_add_co_u32_e32 v180, vcc, s9, v168
	s_waitcnt lgkmcnt(4)
	v_mfma_f32_32x32x16_f16 v[34:49], v[130:133], v[78:81], v[34:49]
	v_addc_co_u32_e32 v181, vcc, 0, v169, vcc
	ds_read_b128 v[130:133], v134 offset:9216
	s_waitcnt lgkmcnt(4)
	v_mfma_f32_32x32x16_f16 v[18:33], v[110:113], v[78:81], v[18:33]
	ds_read_b128 v[110:113], v134 offset:13312
	s_waitcnt lgkmcnt(4)
	v_mfma_f32_32x32x16_f16 v[2:17], v[170:173], v[78:81], v[2:17]
	ds_read_b128 v[78:81], v134 offset:2048
	s_waitcnt vmcnt(11) lgkmcnt(4)
	v_mfma_f32_32x32x16_f16 v[50:65], v[106:109], v[82:85], v[50:65]
	global_load_dwordx4 v[106:109], v[180:181], off offset:1024
	ds_read_b128 v[170:173], v134 offset:6144
	s_waitcnt lgkmcnt(4)
	v_mfma_f32_32x32x16_f16 v[34:49], v[126:129], v[82:85], v[34:49]
	ds_read_b128 v[126:129], v134 offset:10240
	s_waitcnt lgkmcnt(4)
	v_mfma_f32_32x32x16_f16 v[18:33], v[130:133], v[82:85], v[18:33]
	ds_read_b128 v[130:133], v134 offset:14336
	s_waitcnt lgkmcnt(4)
	v_mfma_f32_32x32x16_f16 v[2:17], v[110:113], v[82:85], v[2:17]
	ds_read_b128 v[110:113], v134 offset:3072
	s_waitcnt vmcnt(11) lgkmcnt(4)
	v_mfma_f32_32x32x16_f16 v[50:65], v[78:81], v[98:101], v[50:65]
	global_load_dwordx4 v[82:85], v[180:181], off offset:2048
	ds_read_b128 v[174:177], v134 offset:7168
	s_waitcnt lgkmcnt(4)
	v_mfma_f32_32x32x16_f16 v[34:49], v[170:173], v[98:101], v[34:49]
	ds_read_b128 v[170:173], v134 offset:11264
	s_waitcnt lgkmcnt(4)
	v_mfma_f32_32x32x16_f16 v[18:33], v[126:129], v[98:101], v[18:33]
	ds_read_b128 v[126:129], v134 offset:15360
	s_waitcnt lgkmcnt(4)
	v_mfma_f32_32x32x16_f16 v[2:17], v[130:133], v[98:101], v[2:17]
	global_load_dwordx4 v[78:81], v[180:181], off offset:3072
	s_waitcnt vmcnt(12) lgkmcnt(3)
	v_mfma_f32_32x32x16_f16 v[50:65], v[110:113], v[74:77], v[50:65]
	s_waitcnt lgkmcnt(0)
	s_barrier
	ds_read_b128 v[98:101], v134 offset:16384
	ds_read_b128 v[110:113], v134 offset:20480
	v_mfma_f32_32x32x16_f16 v[34:49], v[174:177], v[74:77], v[34:49]
	ds_read_b128 v[130:133], v134 offset:24576
	v_mfma_f32_32x32x16_f16 v[18:33], v[170:173], v[74:77], v[18:33]
	ds_read_b128 v[170:173], v134 offset:28672
	v_mfma_f32_32x32x16_f16 v[2:17], v[126:129], v[74:77], v[2:17]
	ds_read_b128 v[74:77], v134 offset:17408
	s_waitcnt vmcnt(11) lgkmcnt(4)
	v_mfma_f32_32x32x16_f16 v[50:65], v[98:101], v[114:117], v[50:65]
	global_load_dwordx4 v[98:101], v[178:179], off
	ds_read_b128 v[126:129], v134 offset:21504
	s_waitcnt lgkmcnt(4)
	v_mfma_f32_32x32x16_f16 v[34:49], v[110:113], v[114:117], v[34:49]
	ds_read_b128 v[174:177], v134 offset:25600
	s_waitcnt lgkmcnt(4)
	v_mfma_f32_32x32x16_f16 v[18:33], v[130:133], v[114:117], v[18:33]
	ds_read_b128 v[130:133], v134 offset:29696
	s_waitcnt lgkmcnt(4)
	v_mfma_f32_32x32x16_f16 v[2:17], v[170:173], v[114:117], v[2:17]
	ds_read_b128 v[114:117], v134 offset:18432
	s_waitcnt vmcnt(11) lgkmcnt(4)
	v_mfma_f32_32x32x16_f16 v[50:65], v[74:77], v[118:121], v[50:65]
	global_load_dwordx4 v[110:113], v[178:179], off offset:1024
	ds_read_b128 v[74:77], v134 offset:22528
	s_waitcnt lgkmcnt(4)
	v_mfma_f32_32x32x16_f16 v[34:49], v[126:129], v[118:121], v[34:49]
	ds_read_b128 v[126:129], v134 offset:26624
	s_waitcnt lgkmcnt(4)
	v_mfma_f32_32x32x16_f16 v[18:33], v[174:177], v[118:121], v[18:33]
	ds_read_b128 v[170:173], v134 offset:30720
	s_waitcnt lgkmcnt(4)
	v_mfma_f32_32x32x16_f16 v[2:17], v[130:133], v[118:121], v[2:17]
	ds_read_b128 v[118:121], v134 offset:19456
	s_waitcnt vmcnt(11) lgkmcnt(4)
	v_mfma_f32_32x32x16_f16 v[50:65], v[114:117], v[122:125], v[50:65]
	global_load_dwordx4 v[114:117], v[178:179], off offset:2048
	ds_read_b128 v[130:133], v134 offset:23552
	s_waitcnt lgkmcnt(4)
	v_mfma_f32_32x32x16_f16 v[34:49], v[74:77], v[122:125], v[34:49]
	ds_read_b128 v[174:177], v134 offset:27648
	s_waitcnt lgkmcnt(4)
	v_mfma_f32_32x32x16_f16 v[18:33], v[126:129], v[122:125], v[18:33]
	ds_read_b128 v[126:129], v134 offset:31744
	s_waitcnt lgkmcnt(4)
	v_mfma_f32_32x32x16_f16 v[2:17], v[170:173], v[122:125], v[2:17]
	global_load_dwordx4 v[74:77], v[178:179], off offset:3072
	s_waitcnt vmcnt(12) lgkmcnt(3)
	v_mfma_f32_32x32x16_f16 v[50:65], v[118:121], v[94:97], v[50:65]
	s_waitcnt lgkmcnt(0)
	s_barrier
	ds_read_b128 v[118:121], v134
	ds_read_b128 v[122:125], v134 offset:4096
	v_mfma_f32_32x32x16_f16 v[34:49], v[130:133], v[94:97], v[34:49]
	ds_read_b128 v[130:133], v134 offset:8192
	v_mfma_f32_32x32x16_f16 v[18:33], v[174:177], v[94:97], v[18:33]
	v_mfma_f32_32x32x16_f16 v[2:17], v[126:129], v[94:97], v[2:17]
	ds_read_b128 v[126:129], v134 offset:12288
	ds_read_b128 v[170:173], v134 offset:1024
	s_waitcnt vmcnt(11) lgkmcnt(4)
	v_mfma_f32_32x32x16_f16 v[50:65], v[118:121], v[102:105], v[50:65]
	s_mov_b32 s9, 0xf000
	v_add_co_u32_e32 v174, vcc, s9, v168
	ds_read_b128 v[118:121], v134 offset:5120
	s_nop 0
	v_addc_co_u32_e32 v175, vcc, 0, v169, vcc
	global_load_dwordx4 v[94:97], v[174:175], off
	s_waitcnt lgkmcnt(4)
	v_mfma_f32_32x32x16_f16 v[34:49], v[122:125], v[102:105], v[34:49]
	ds_read_b128 v[122:125], v134 offset:9216
	s_waitcnt lgkmcnt(4)
	v_mfma_f32_32x32x16_f16 v[18:33], v[130:133], v[102:105], v[18:33]
	s_waitcnt lgkmcnt(3)
	v_mfma_f32_32x32x16_f16 v[2:17], v[126:129], v[102:105], v[2:17]
	ds_read_b128 v[126:129], v134 offset:13312
	ds_read_b128 v[130:133], v134 offset:2048
	s_waitcnt vmcnt(11) lgkmcnt(4)
	v_mfma_f32_32x32x16_f16 v[50:65], v[170:173], v[86:89], v[50:65]
	global_load_dwordx4 v[102:105], v[174:175], off offset:1024
	s_waitcnt lgkmcnt(3)
	v_mfma_f32_32x32x16_f16 v[34:49], v[118:121], v[86:89], v[34:49]
	ds_read_b128 v[118:121], v134 offset:6144
	s_waitcnt lgkmcnt(3)
	v_mfma_f32_32x32x16_f16 v[18:33], v[122:125], v[86:89], v[18:33]
	ds_read_b128 v[122:125], v134 offset:10240
	s_waitcnt lgkmcnt(3)
	v_mfma_f32_32x32x16_f16 v[2:17], v[126:129], v[86:89], v[2:17]
	ds_read_b128 v[126:129], v134 offset:14336
	ds_read_b128 v[168:171], v134 offset:3072
	s_waitcnt vmcnt(11) lgkmcnt(4)
	v_mfma_f32_32x32x16_f16 v[50:65], v[130:133], v[70:73], v[50:65]
	global_load_dwordx4 v[86:89], v[174:175], off offset:2048
	s_waitcnt lgkmcnt(3)
	v_mfma_f32_32x32x16_f16 v[34:49], v[118:121], v[70:73], v[34:49]
	ds_read_b128 v[118:121], v134 offset:7168
	s_waitcnt lgkmcnt(3)
	v_mfma_f32_32x32x16_f16 v[18:33], v[122:125], v[70:73], v[18:33]
	ds_read_b128 v[122:125], v134 offset:11264
	s_waitcnt lgkmcnt(3)
	v_mfma_f32_32x32x16_f16 v[2:17], v[126:129], v[70:73], v[2:17]
	ds_read_b128 v[126:129], v134 offset:15360
	global_load_dwordx4 v[70:73], v[174:175], off offset:3072
	s_waitcnt vmcnt(12) lgkmcnt(3)
	v_mfma_f32_32x32x16_f16 v[50:65], v[168:171], v[66:69], v[50:65]
	s_waitcnt lgkmcnt(0)
	s_barrier
	ds_read_b128 v[130:133], v134 offset:16384
	v_mfma_f32_32x32x16_f16 v[34:49], v[118:121], v[66:69], v[34:49]
	ds_read_b128 v[118:121], v134 offset:20480
	v_mfma_f32_32x32x16_f16 v[18:33], v[122:125], v[66:69], v[18:33]
	ds_read_b128 v[122:125], v134 offset:24576
	v_mfma_f32_32x32x16_f16 v[2:17], v[126:129], v[66:69], v[2:17]
	ds_read_b128 v[66:69], v134 offset:28672
	ds_read_b128 v[126:129], v134 offset:17408
	s_waitcnt vmcnt(11) lgkmcnt(4)
	v_mfma_f32_32x32x16_f16 v[50:65], v[130:133], v[90:93], v[50:65]
	ds_read_b128 v[130:133], v134 offset:21504
	s_waitcnt lgkmcnt(4)
	v_mfma_f32_32x32x16_f16 v[34:49], v[118:121], v[90:93], v[34:49]
	ds_read_b128 v[118:121], v134 offset:25600
	s_waitcnt lgkmcnt(4)
	v_mfma_f32_32x32x16_f16 v[18:33], v[122:125], v[90:93], v[18:33]
	ds_read_b128 v[122:125], v134 offset:29696
	s_waitcnt lgkmcnt(4)
	v_mfma_f32_32x32x16_f16 v[2:17], v[66:69], v[90:93], v[2:17]
	ds_read_b128 v[66:69], v134 offset:18432
	s_waitcnt vmcnt(10) lgkmcnt(4)
	v_mfma_f32_32x32x16_f16 v[50:65], v[126:129], v[106:109], v[50:65]
	ds_read_b128 v[90:93], v134 offset:22528
	s_waitcnt lgkmcnt(4)
	v_mfma_f32_32x32x16_f16 v[34:49], v[130:133], v[106:109], v[34:49]
	ds_read_b128 v[126:129], v134 offset:26624
	s_waitcnt lgkmcnt(4)
	v_mfma_f32_32x32x16_f16 v[18:33], v[118:121], v[106:109], v[18:33]
	ds_read_b128 v[118:121], v134 offset:30720
	s_waitcnt lgkmcnt(4)
	v_mfma_f32_32x32x16_f16 v[2:17], v[122:125], v[106:109], v[2:17]
	ds_read_b128 v[106:109], v134 offset:19456
	s_waitcnt vmcnt(9) lgkmcnt(4)
	v_mfma_f32_32x32x16_f16 v[50:65], v[66:69], v[82:85], v[50:65]
	ds_read_b128 v[66:69], v134 offset:23552
	s_waitcnt lgkmcnt(4)
	v_mfma_f32_32x32x16_f16 v[34:49], v[90:93], v[82:85], v[34:49]
	ds_read_b128 v[90:93], v134 offset:27648
	s_waitcnt lgkmcnt(4)
	v_mfma_f32_32x32x16_f16 v[18:33], v[126:129], v[82:85], v[18:33]
	ds_read_b128 v[122:125], v134 offset:31744
	s_waitcnt lgkmcnt(4)
	v_mfma_f32_32x32x16_f16 v[2:17], v[118:121], v[82:85], v[2:17]
	s_waitcnt vmcnt(8) lgkmcnt(3)
	v_mfma_f32_32x32x16_f16 v[50:65], v[106:109], v[78:81], v[50:65]
	s_waitcnt lgkmcnt(0)
	s_barrier
	ds_read_b128 v[82:85], v134
	ds_read_b128 v[106:109], v134 offset:4096
	v_mfma_f32_32x32x16_f16 v[34:49], v[66:69], v[78:81], v[34:49]
	ds_read_b128 v[66:69], v134 offset:8192
	v_mfma_f32_32x32x16_f16 v[18:33], v[90:93], v[78:81], v[18:33]
	ds_read_b128 v[90:93], v134 offset:12288
	v_mfma_f32_32x32x16_f16 v[2:17], v[122:125], v[78:81], v[2:17]
	ds_read_b128 v[78:81], v134 offset:1024
	s_waitcnt vmcnt(7) lgkmcnt(4)
	v_mfma_f32_32x32x16_f16 v[50:65], v[82:85], v[98:101], v[50:65]
	ds_read_b128 v[82:85], v134 offset:5120
	s_waitcnt lgkmcnt(4)
	v_mfma_f32_32x32x16_f16 v[34:49], v[106:109], v[98:101], v[34:49]
	ds_read_b128 v[106:109], v134 offset:9216
	s_waitcnt lgkmcnt(4)
	v_mfma_f32_32x32x16_f16 v[18:33], v[66:69], v[98:101], v[18:33]
	ds_read_b128 v[66:69], v134 offset:13312
	s_waitcnt lgkmcnt(4)
	v_mfma_f32_32x32x16_f16 v[2:17], v[90:93], v[98:101], v[2:17]
	ds_read_b128 v[90:93], v134 offset:2048
	s_waitcnt vmcnt(6) lgkmcnt(4)
	v_mfma_f32_32x32x16_f16 v[50:65], v[78:81], v[110:113], v[50:65]
	ds_read_b128 v[78:81], v134 offset:6144
	s_waitcnt lgkmcnt(4)
	v_mfma_f32_32x32x16_f16 v[34:49], v[82:85], v[110:113], v[34:49]
	ds_read_b128 v[82:85], v134 offset:10240
	s_waitcnt lgkmcnt(4)
	v_mfma_f32_32x32x16_f16 v[18:33], v[106:109], v[110:113], v[18:33]
	ds_read_b128 v[98:101], v134 offset:14336
	s_waitcnt lgkmcnt(4)
	v_mfma_f32_32x32x16_f16 v[2:17], v[66:69], v[110:113], v[2:17]
	ds_read_b128 v[66:69], v134 offset:3072
	s_waitcnt vmcnt(5) lgkmcnt(4)
	v_mfma_f32_32x32x16_f16 v[50:65], v[90:93], v[114:117], v[50:65]
	ds_read_b128 v[90:93], v134 offset:7168
	s_waitcnt lgkmcnt(4)
	v_mfma_f32_32x32x16_f16 v[34:49], v[78:81], v[114:117], v[34:49]
	ds_read_b128 v[78:81], v134 offset:11264
	s_waitcnt lgkmcnt(4)
	v_mfma_f32_32x32x16_f16 v[18:33], v[82:85], v[114:117], v[18:33]
	ds_read_b128 v[82:85], v134 offset:15360
	s_waitcnt lgkmcnt(4)
	v_mfma_f32_32x32x16_f16 v[2:17], v[98:101], v[114:117], v[2:17]
	s_waitcnt vmcnt(4) lgkmcnt(3)
	v_mfma_f32_32x32x16_f16 v[50:65], v[66:69], v[74:77], v[50:65]
	s_waitcnt lgkmcnt(0)
	s_barrier
	ds_read_b128 v[66:69], v134 offset:16384
	ds_read_b128 v[98:101], v134 offset:20480
	v_mfma_f32_32x32x16_f16 v[34:49], v[90:93], v[74:77], v[34:49]
	ds_read_b128 v[90:93], v134 offset:24576
	v_mfma_f32_32x32x16_f16 v[18:33], v[78:81], v[74:77], v[18:33]
	ds_read_b128 v[78:81], v134 offset:28672
	v_mfma_f32_32x32x16_f16 v[2:17], v[82:85], v[74:77], v[2:17]
	ds_read_b128 v[74:77], v134 offset:17408
	s_waitcnt vmcnt(3) lgkmcnt(4)
	v_mfma_f32_32x32x16_f16 v[50:65], v[66:69], v[94:97], v[50:65]
	ds_read_b128 v[66:69], v134 offset:21504
	s_waitcnt lgkmcnt(4)
	v_mfma_f32_32x32x16_f16 v[34:49], v[98:101], v[94:97], v[34:49]
	ds_read_b128 v[82:85], v134 offset:25600
	s_waitcnt lgkmcnt(4)
	v_mfma_f32_32x32x16_f16 v[18:33], v[90:93], v[94:97], v[18:33]
	ds_read_b128 v[90:93], v134 offset:29696
	s_waitcnt lgkmcnt(4)
	v_mfma_f32_32x32x16_f16 v[2:17], v[78:81], v[94:97], v[2:17]
	s_waitcnt vmcnt(2) lgkmcnt(3)
	v_mfma_f32_32x32x16_f16 v[50:65], v[74:77], v[102:105], v[50:65]
	ds_read_b128 v[74:77], v134 offset:18432
	s_waitcnt lgkmcnt(3)
	v_mfma_f32_32x32x16_f16 v[34:49], v[66:69], v[102:105], v[34:49]
	ds_read_b128 v[66:69], v134 offset:22528
	ds_read_b128 v[78:81], v134 offset:26624
	s_waitcnt lgkmcnt(4)
	v_mfma_f32_32x32x16_f16 v[18:33], v[82:85], v[102:105], v[18:33]
	ds_read_b128 v[82:85], v134 offset:30720
	s_waitcnt lgkmcnt(4)
	v_mfma_f32_32x32x16_f16 v[2:17], v[90:93], v[102:105], v[2:17]
	ds_read_b128 v[90:93], v134 offset:19456
	s_waitcnt vmcnt(1) lgkmcnt(4)
	v_mfma_f32_32x32x16_f16 v[50:65], v[74:77], v[86:89], v[50:65]
	ds_read_b128 v[74:77], v134 offset:23552
	s_waitcnt lgkmcnt(4)
	v_mfma_f32_32x32x16_f16 v[34:49], v[66:69], v[86:89], v[34:49]
	ds_read_b128 v[66:69], v134 offset:27648
	s_waitcnt lgkmcnt(4)
	v_mfma_f32_32x32x16_f16 v[18:33], v[78:81], v[86:89], v[18:33]
	ds_read_b128 v[78:81], v134 offset:31744
	s_waitcnt lgkmcnt(4)
	v_mfma_f32_32x32x16_f16 v[2:17], v[82:85], v[86:89], v[2:17]
	s_waitcnt vmcnt(0) lgkmcnt(3)
	v_mfma_f32_32x32x16_f16 v[50:65], v[90:93], v[70:73], v[50:65]
	s_waitcnt lgkmcnt(2)
	v_mfma_f32_32x32x16_f16 v[34:49], v[74:77], v[70:73], v[34:49]
	s_waitcnt lgkmcnt(1)
	v_mfma_f32_32x32x16_f16 v[18:33], v[66:69], v[70:73], v[18:33]
	s_waitcnt lgkmcnt(0)
	v_mfma_f32_32x32x16_f16 v[2:17], v[78:81], v[70:73], v[2:17]
	v_cvt_f32_f16_e32 v66, v166
	v_cvt_f32_f16_sdwa v67, v166 dst_sel:DWORD dst_unused:UNUSED_PAD src0_sel:WORD_1
	v_cvt_f32_f16_e32 v68, v167
	v_cvt_f32_f16_sdwa v69, v167 dst_sel:DWORD dst_unused:UNUSED_PAD src0_sel:WORD_1
	v_cvt_f32_f16_e32 v70, v164
	v_cvt_f32_f16_sdwa v71, v164 dst_sel:DWORD dst_unused:UNUSED_PAD src0_sel:WORD_1
	v_cvt_f32_f16_e32 v72, v165
	v_cvt_f32_f16_sdwa v73, v165 dst_sel:DWORD dst_unused:UNUSED_PAD src0_sel:WORD_1
	v_cvt_f32_f16_e32 v74, v162
	v_cvt_f32_f16_sdwa v75, v162 dst_sel:DWORD dst_unused:UNUSED_PAD src0_sel:WORD_1
	v_pk_fma_f32 v[66:67], v[66:67], v[66:67], 1.0 op_sel_hi:[1,1,0] neg_lo:[1,0,0] neg_hi:[1,0,0]
	v_cvt_f32_f16_e32 v76, v163
	v_cvt_f32_f16_sdwa v77, v163 dst_sel:DWORD dst_unused:UNUSED_PAD src0_sel:WORD_1
	v_pk_mul_f32 v[66:67], v[50:51], v[66:67]
	v_pk_fma_f32 v[50:51], v[68:69], v[68:69], 1.0 op_sel_hi:[1,1,0] neg_lo:[1,0,0] neg_hi:[1,0,0]
	s_nop 0
	v_pk_mul_f32 v[68:69], v[52:53], v[50:51]
	v_pk_fma_f32 v[50:51], v[70:71], v[70:71], 1.0 op_sel_hi:[1,1,0] neg_lo:[1,0,0] neg_hi:[1,0,0]
	s_barrier
	v_pk_mul_f32 v[54:55], v[54:55], v[50:51]
	v_pk_fma_f32 v[50:51], v[72:73], v[72:73], 1.0 op_sel_hi:[1,1,0] neg_lo:[1,0,0] neg_hi:[1,0,0]
	s_nop 0
	v_pk_mul_f32 v[56:57], v[56:57], v[50:51]
	v_pk_fma_f32 v[50:51], v[74:75], v[74:75], 1.0 op_sel_hi:[1,1,0] neg_lo:[1,0,0] neg_hi:[1,0,0]
	v_cvt_f32_f16_e32 v78, v160
	v_pk_mul_f32 v[90:91], v[58:59], v[50:51]
	v_pk_fma_f32 v[50:51], v[76:77], v[76:77], 1.0 op_sel_hi:[1,1,0] neg_lo:[1,0,0] neg_hi:[1,0,0]
	v_cvt_f32_f16_sdwa v79, v160 dst_sel:DWORD dst_unused:UNUSED_PAD src0_sel:WORD_1
	v_pk_mul_f32 v[92:93], v[60:61], v[50:51]
	ds_read_b128 v[50:53], v134 offset:33792
	v_cvt_f32_f16_e32 v86, v161
	v_cvt_f32_f16_sdwa v87, v161 dst_sel:DWORD dst_unused:UNUSED_PAD src0_sel:WORD_1
	v_cvt_pk_f16_f32 v57, v56, v57
	v_cvt_pk_f16_f32 v56, v54, v55
	v_cvt_pk_f16_f32 v55, v68, v69
	v_cvt_pk_f16_f32 v54, v66, v67
	v_pk_fma_f32 v[58:59], v[78:79], v[78:79], 1.0 op_sel_hi:[1,1,0] neg_lo:[1,0,0] neg_hi:[1,0,0]
	v_cvt_f32_f16_e32 v94, v152
	s_waitcnt lgkmcnt(0)
	v_mfma_f32_32x32x16_f16 v[66:81], v[50:53], v[54:57], 0
	v_fma_f32 v50, -v86, v86, 1.0
	v_fma_f32 v51, -v87, v87, 1.0
	v_mul_f32_e64 v62, v62, v58
	v_mul_f32_e64 v63, v63, v59
	ds_read_b128 v[58:61], v134 offset:34816
	ds_read_b128 v[82:85], v134 offset:35840
	v_mul_f32_e32 v50, v64, v50
	v_mul_f32_e32 v51, v65, v51
	v_cvt_f32_f16_e32 v52, v159
	v_cvt_pk_f16_f32 v89, v50, v51
	v_cvt_f32_f16_e32 v50, v158
	v_cvt_f32_f16_sdwa v51, v158 dst_sel:DWORD dst_unused:UNUSED_PAD src0_sel:WORD_1
	v_cvt_f32_f16_sdwa v53, v159 dst_sel:DWORD dst_unused:UNUSED_PAD src0_sel:WORD_1
	v_cvt_pk_f16_f32 v88, v62, v63
	v_cvt_f32_f16_e32 v62, v156
	v_cvt_f32_f16_sdwa v63, v156 dst_sel:DWORD dst_unused:UNUSED_PAD src0_sel:WORD_1
	v_cvt_pk_f16_f32 v87, v92, v93
	v_cvt_pk_f16_f32 v86, v90, v91
	v_cvt_f32_f16_e32 v64, v157
	v_cvt_f32_f16_sdwa v65, v157 dst_sel:DWORD dst_unused:UNUSED_PAD src0_sel:WORD_1
	s_waitcnt lgkmcnt(0)
	v_mfma_f32_32x32x16_f16 v[66:81], v[82:85], v[86:89], v[66:81]
	v_cvt_f32_f16_e32 v82, v154
	v_cvt_f32_f16_sdwa v83, v154 dst_sel:DWORD dst_unused:UNUSED_PAD src0_sel:WORD_1
	v_fma_f32 v50, -v50, v50, 1.0
	v_fma_f32 v51, -v51, v51, 1.0
	v_cvt_f32_f16_e32 v84, v155
	v_cvt_f32_f16_sdwa v85, v155 dst_sel:DWORD dst_unused:UNUSED_PAD src0_sel:WORD_1
	v_mul_f32_e32 v98, v34, v50
	v_mul_f32_e32 v99, v35, v51
	v_fma_f32 v34, -v52, v52, 1.0
	v_fma_f32 v35, -v53, v53, 1.0
	v_cvt_f32_f16_sdwa v95, v152 dst_sel:DWORD dst_unused:UNUSED_PAD src0_sel:WORD_1
	v_mul_f32_e32 v100, v36, v34
	v_mul_f32_e32 v101, v37, v35
	v_fma_f32 v34, -v62, v62, 1.0
	v_fma_f32 v35, -v63, v63, 1.0
	ds_read_b128 v[90:93], v134 offset:36864
	v_mul_f32_e32 v38, v38, v34
	v_mul_f32_e32 v39, v39, v35
	v_fma_f32 v34, -v64, v64, 1.0
	v_fma_f32 v35, -v65, v65, 1.0
	v_mfma_f32_32x32x16_f16 v[50:65], v[58:61], v[54:57], 0
	v_mul_f32_e64 v40, v40, v34
	v_mul_f32_e64 v41, v41, v35
	v_fma_f32 v34, -v82, v82, 1.0
	v_fma_f32 v35, -v83, v83, 1.0
	v_cvt_pk_f16_f32 v41, v40, v41
	v_mul_f32_e32 v82, v42, v34
	v_mul_f32_e32 v83, v43, v35
	v_fma_f32 v34, -v84, v84, 1.0
	v_fma_f32 v35, -v85, v85, 1.0
	v_cvt_pk_f16_f32 v40, v38, v39
	v_mul_f32_e32 v84, v44, v34
	v_mul_f32_e32 v85, v45, v35
	v_fma_f32 v34, -v94, v94, 1.0
	v_fma_f32 v35, -v95, v95, 1.0
	v_cvt_pk_f16_f32 v39, v100, v101
	v_mul_f32_e32 v46, v46, v34
	v_mul_f32_e32 v47, v47, v35
	ds_read_b128 v[34:37], v134 offset:37888
	v_cvt_pk_f16_f32 v38, v98, v99
	v_cvt_f32_f16_e32 v96, v153
	v_cvt_f32_f16_sdwa v97, v153 dst_sel:DWORD dst_unused:UNUSED_PAD src0_sel:WORD_1
	s_waitcnt lgkmcnt(0)
	v_mfma_f32_32x32x16_f16 v[66:81], v[34:37], v[38:41], v[66:81]
	v_cvt_f32_f16_e32 v34, v150
	v_cvt_f32_f16_sdwa v35, v150 dst_sel:DWORD dst_unused:UNUSED_PAD src0_sel:WORD_1
	v_cvt_f32_f16_e32 v36, v151
	v_cvt_f32_f16_sdwa v37, v151 dst_sel:DWORD dst_unused:UNUSED_PAD src0_sel:WORD_1
	v_fma_f32 v42, -v96, v96, 1.0
	v_fma_f32 v43, -v97, v97, 1.0
	v_fma_f32 v34, -v34, v34, 1.0
	v_fma_f32 v35, -v35, v35, 1.0
	v_mul_f32_e32 v48, v48, v42
	v_mul_f32_e32 v49, v49, v43
	v_mfma_f32_32x32x16_f16 v[50:65], v[90:93], v[86:89], v[50:65]
	v_cvt_f32_f16_e32 v86, v148
	v_cvt_f32_f16_sdwa v87, v148 dst_sel:DWORD dst_unused:UNUSED_PAD src0_sel:WORD_1
	v_cvt_f32_f16_e32 v88, v149
	v_cvt_f32_f16_sdwa v89, v149 dst_sel:DWORD dst_unused:UNUSED_PAD src0_sel:WORD_1
	v_cvt_f32_f16_e32 v90, v146
	v_cvt_f32_f16_sdwa v91, v146 dst_sel:DWORD dst_unused:UNUSED_PAD src0_sel:WORD_1
	ds_read_b128 v[42:45], v134 offset:38912
	v_cvt_f32_f16_e32 v92, v147
	v_cvt_f32_f16_sdwa v93, v147 dst_sel:DWORD dst_unused:UNUSED_PAD src0_sel:WORD_1
	v_mul_f32_e32 v34, v18, v34
	v_mul_f32_e32 v35, v19, v35
	v_fma_f32 v18, -v36, v36, 1.0
	v_fma_f32 v19, -v37, v37, 1.0
	v_cvt_f32_f16_e32 v94, v144
	v_cvt_f32_f16_sdwa v95, v144 dst_sel:DWORD dst_unused:UNUSED_PAD src0_sel:WORD_1
	v_mul_f32_e32 v36, v20, v18
	v_mul_f32_e32 v37, v21, v19
	v_fma_f32 v18, -v86, v86, 1.0
	v_fma_f32 v19, -v87, v87, 1.0
	v_cvt_f32_f16_e32 v96, v145
	v_mul_f32_e32 v86, v22, v18
	v_mul_f32_e32 v87, v23, v19
	v_fma_f32 v18, -v88, v88, 1.0
	v_fma_f32 v19, -v89, v89, 1.0
	v_cvt_f32_f16_sdwa v97, v145 dst_sel:DWORD dst_unused:UNUSED_PAD src0_sel:WORD_1
	v_mul_f32_e32 v88, v24, v18
	v_mul_f32_e32 v89, v25, v19
	v_fma_f32 v18, -v90, v90, 1.0
	v_fma_f32 v19, -v91, v91, 1.0
	v_cvt_pk_f16_f32 v25, v48, v49
	v_mul_f32_e32 v90, v26, v18
	v_mul_f32_e32 v91, v27, v19
	v_fma_f32 v18, -v92, v92, 1.0
	v_fma_f32 v19, -v93, v93, 1.0
	v_cvt_pk_f16_f32 v24, v46, v47
	v_mul_f32_e32 v92, v28, v18
	v_mul_f32_e32 v93, v29, v19
	v_fma_f32 v18, -v94, v94, 1.0
	v_fma_f32 v19, -v95, v95, 1.0
	ds_read_b128 v[26:29], v134 offset:40960
	v_mul_f32_e32 v30, v30, v18
	v_mul_f32_e32 v31, v31, v19
	ds_read_b128 v[18:21], v134 offset:39936
	s_waitcnt lgkmcnt(2)
	v_mfma_f32_32x32x16_f16 v[50:65], v[42:45], v[38:41], v[50:65]
	v_cvt_f32_f16_e32 v40, v142
	v_cvt_f32_f16_sdwa v41, v142 dst_sel:DWORD dst_unused:UNUSED_PAD src0_sel:WORD_1
	v_fma_f32 v38, -v96, v96, 1.0
	v_fma_f32 v39, -v97, v97, 1.0
	v_cvt_pk_f16_f32 v23, v84, v85
	v_cvt_pk_f16_f32 v22, v82, v83
	v_mul_f32_e32 v32, v32, v38
	v_mul_f32_e32 v33, v33, v39
	v_cvt_f32_f16_e32 v38, v143
	s_waitcnt lgkmcnt(0)
	v_mfma_f32_32x32x16_f16 v[66:81], v[18:21], v[22:25], v[66:81]
	v_cvt_f32_f16_sdwa v39, v143 dst_sel:DWORD dst_unused:UNUSED_PAD src0_sel:WORD_1
	v_fma_f32 v18, -v40, v40, 1.0
	v_fma_f32 v19, -v41, v41, 1.0
	s_or_b32 s6, s6, s7
	v_mul_f32_e64 v40, v2, v18
	v_mul_f32_e64 v41, v3, v19
	ds_read_b128 v[18:21], v134 offset:41984
	v_fma_f32 v2, -v38, v38, 1.0
	v_fma_f32 v3, -v39, v39, 1.0
	v_cvt_f32_f16_e32 v38, v140
	v_mfma_f32_32x32x16_f16 v[50:65], v[26:29], v[22:25], v[50:65]
	ds_read_b128 v[26:29], v134 offset:43008
	v_cvt_f32_f16_sdwa v39, v140 dst_sel:DWORD dst_unused:UNUSED_PAD src0_sel:WORD_1
	v_cvt_pk_f16_f32 v22, v34, v35
	v_mul_f32_e64 v34, v4, v2
	v_mul_f32_e64 v35, v5, v3
	v_cvt_pk_f16_f32 v25, v88, v89
	v_fma_f32 v2, -v38, v38, 1.0
	v_fma_f32 v3, -v39, v39, 1.0
	v_cvt_pk_f16_f32 v24, v86, v87
	v_cvt_pk_f16_f32 v23, v36, v37
	v_mul_f32_e32 v6, v6, v2
	v_mul_f32_e32 v7, v7, v3
	ds_read_b128 v[2:5], v134 offset:44032
	s_waitcnt lgkmcnt(2)
	v_mfma_f32_32x32x16_f16 v[66:81], v[18:21], v[22:25], v[66:81]
	v_cvt_f32_f16_e32 v18, v141
	v_cvt_f32_f16_sdwa v19, v141 dst_sel:DWORD dst_unused:UNUSED_PAD src0_sel:WORD_1
	v_cvt_pk_f16_f32 v21, v32, v33
	v_cvt_pk_f16_f32 v20, v30, v31
	s_ashr_i32 s7, s6, 31
	s_lshl_b64 s[6:7], s[6:7], 12
	s_add_u32 s2, s2, s6
	s_waitcnt lgkmcnt(1)
	v_mfma_f32_32x32x16_f16 v[50:65], v[26:29], v[22:25], v[50:65]
	ds_read_b128 v[22:25], v134 offset:45056
	v_cvt_f32_f16_e32 v28, v138
	v_cvt_f32_f16_sdwa v29, v138 dst_sel:DWORD dst_unused:UNUSED_PAD src0_sel:WORD_1
	v_fma_f32 v26, -v18, v18, 1.0
	v_fma_f32 v27, -v19, v19, 1.0
	v_cvt_pk_f16_f32 v19, v92, v93
	v_cvt_pk_f16_f32 v18, v90, v91
	v_mul_f32_e32 v8, v8, v26
	v_mul_f32_e32 v9, v9, v27
	v_cvt_f32_f16_e32 v26, v139
	s_waitcnt lgkmcnt(1)
	v_mfma_f32_32x32x16_f16 v[66:81], v[2:5], v[18:21], v[66:81]
	v_fma_f32 v2, -v28, v28, 1.0
	v_fma_f32 v3, -v29, v29, 1.0
	v_cvt_f32_f16_sdwa v27, v139 dst_sel:DWORD dst_unused:UNUSED_PAD src0_sel:WORD_1
	v_mul_f32_e64 v10, v10, v2
	v_mul_f32_e64 v11, v11, v3
	ds_read_b128 v[2:5], v134 offset:46080
	v_cvt_pk_f16_f32 v9, v8, v9
	v_cvt_pk_f16_f32 v8, v6, v7
	v_cvt_pk_f16_f32 v7, v34, v35
	s_waitcnt lgkmcnt(1)
	v_mfma_f32_32x32x16_f16 v[50:65], v[22:25], v[18:21], v[50:65]
	ds_read_b128 v[18:21], v134 offset:47104
	v_fma_f32 v22, -v26, v26, 1.0
	v_fma_f32 v23, -v27, v27, 1.0
	v_cvt_f32_f16_e32 v24, v136
	v_cvt_f32_f16_sdwa v25, v136 dst_sel:DWORD dst_unused:UNUSED_PAD src0_sel:WORD_1
	v_mul_f32_e32 v12, v12, v22
	v_mul_f32_e32 v13, v13, v23
	v_cvt_f32_f16_e32 v22, v137
	v_cvt_f32_f16_sdwa v23, v137 dst_sel:DWORD dst_unused:UNUSED_PAD src0_sel:WORD_1
	v_cvt_pk_f16_f32 v6, v40, v41
	s_addc_u32 s3, s3, s7
	s_waitcnt lgkmcnt(1)
	v_mfma_f32_32x32x16_f16 v[66:81], v[2:5], v[6:9], v[66:81]
	v_fma_f32 v2, -v24, v24, 1.0
	v_fma_f32 v3, -v25, v25, 1.0
	v_mul_f32_e64 v14, v14, v2
	v_mul_f32_e64 v15, v15, v3
	ds_read_b128 v[2:5], v134 offset:48128
	s_waitcnt lgkmcnt(1)
	v_mfma_f32_32x32x16_f16 v[50:65], v[18:21], v[6:9], v[50:65]
	v_fma_f32 v6, -v22, v22, 1.0
	v_fma_f32 v7, -v23, v23, 1.0
	v_cvt_pk_f16_f32 v8, v14, v15
	v_mul_f32_e64 v6, v16, v6
	v_mul_f32_e64 v7, v17, v7
	v_cvt_pk_f16_f32 v9, v6, v7
	v_cvt_pk_f16_f32 v7, v12, v13
	v_cvt_pk_f16_f32 v6, v10, v11
	ds_read_b128 v[10:13], v134 offset:49152
	s_waitcnt lgkmcnt(1)
	v_mfma_f32_32x32x16_f16 v[66:81], v[2:5], v[6:9], v[66:81]
	s_waitcnt lgkmcnt(0)
	v_mfma_f32_32x32x16_f16 v[50:65], v[10:13], v[6:9], v[50:65]
	s_nop 9
	v_cvt_pk_f16_f32 v5, v72, v73
	v_cvt_pk_f16_f32 v4, v70, v71
	v_cvt_pk_f16_f32 v3, v68, v69
	v_cvt_pk_f16_f32 v2, v66, v67
	global_store_dwordx4 v134, v[2:5], s[2:3] sc1
	s_nop 1
	v_cvt_pk_f16_f32 v5, v80, v81
	v_cvt_pk_f16_f32 v4, v78, v79
	v_cvt_pk_f16_f32 v3, v76, v77
	v_cvt_pk_f16_f32 v2, v74, v75
	global_store_dwordx4 v134, v[2:5], s[2:3] offset:1024 sc1
	s_nop 1
	v_cvt_pk_f16_f32 v5, v56, v57
	v_cvt_pk_f16_f32 v4, v54, v55
	v_cvt_pk_f16_f32 v3, v52, v53
	v_cvt_pk_f16_f32 v2, v50, v51
	global_store_dwordx4 v134, v[2:5], s[2:3] offset:2048 sc1
	s_nop 1
	v_cvt_pk_f16_f32 v5, v64, v65
	v_cvt_pk_f16_f32 v4, v62, v63
	v_cvt_pk_f16_f32 v3, v60, v61
	v_cvt_pk_f16_f32 v2, v58, v59
	global_store_dwordx4 v134, v[2:5], s[2:3] offset:3072 sc1
	s_cbranch_execnz .LBB3_2
.LBB3_4:
	s_load_dwordx2 s[6:7], s[0:1], 0x0
	s_load_dwordx2 s[2:3], s[0:1], 0x38
	s_lshr_b32 s0, s8, 6
	s_lshl_b32 s1, s4, 8
	s_lshl_b32 s8, s5, 7
	s_add_i32 s8, s8, s1
	s_ashr_i32 s9, s8, 31
	s_lshl_b64 s[8:9], s[8:9], 10
	s_waitcnt lgkmcnt(0)
	s_add_u32 s6, s6, s8
	s_addc_u32 s7, s7, s9
	v_mov_b32_e32 v135, 0
	v_lshl_add_u64 v[2:3], s[6:7], 0, v[134:135]
	s_mov_b32 s1, 0x10000
	v_add_co_u32_e32 v36, vcc, s1, v2
	s_mov_b32 s1, 0x11000
	s_nop 0
	v_addc_co_u32_e32 v37, vcc, 0, v3, vcc
	v_add_co_u32_e32 v68, vcc, s1, v2
	global_load_dwordx4 v[4:7], v134, s[6:7]
	global_load_dwordx4 v[8:11], v134, s[6:7] offset:1024
	global_load_dwordx4 v[12:15], v134, s[6:7] offset:2048
	v_addc_co_u32_e32 v69, vcc, 0, v3, vcc
	global_load_dwordx4 v[16:19], v134, s[6:7] offset:3072
	global_load_dwordx4 v[20:23], v[68:69], off offset:-4096
	global_load_dwordx4 v[24:27], v[36:37], off offset:1024
	global_load_dwordx4 v[28:31], v[36:37], off offset:2048
	global_load_dwordx4 v[32:35], v[36:37], off offset:3072
	s_movk_i32 s7, 0x2000
	v_add_co_u32_e32 v100, vcc, s7, v2
	s_movk_i32 s6, 0x1000
	s_nop 0
	v_addc_co_u32_e32 v101, vcc, 0, v3, vcc
	v_add_co_u32_e32 v70, vcc, s6, v2
	global_load_dwordx4 v[36:39], v[100:101], off offset:-4096
	s_nop 0
	v_addc_co_u32_e32 v71, vcc, 0, v3, vcc
	global_load_dwordx4 v[40:43], v[70:71], off offset:1024
	global_load_dwordx4 v[44:47], v[70:71], off offset:2048
	global_load_dwordx4 v[48:51], v[70:71], off offset:3072
	global_load_dwordx4 v[52:55], v[68:69], off
	global_load_dwordx4 v[56:59], v[68:69], off offset:1024
	global_load_dwordx4 v[60:63], v[68:69], off offset:2048
	global_load_dwordx4 v[64:67], v[68:69], off offset:3072
	s_mov_b32 s1, 0x12000
	v_add_co_u32_e32 v102, vcc, s1, v2
	s_mov_b32 s8, 0x13000
	s_nop 0
	v_addc_co_u32_e32 v103, vcc, 0, v3, vcc
	v_add_co_u32_e32 v104, vcc, s8, v2
	s_movk_i32 s9, 0x4000
	s_nop 0
	v_addc_co_u32_e32 v105, vcc, 0, v3, vcc
	v_add_co_u32_e32 v106, vcc, s9, v2
	global_load_dwordx4 v[68:71], v[100:101], off
	global_load_dwordx4 v[72:75], v[100:101], off offset:1024
	global_load_dwordx4 v[76:79], v[100:101], off offset:2048
	global_load_dwordx4 v[80:83], v[100:101], off offset:3072
	global_load_dwordx4 v[84:87], v[104:105], off offset:-4096
	global_load_dwordx4 v[88:91], v[102:103], off offset:1024
	global_load_dwordx4 v[92:95], v[102:103], off offset:2048
	global_load_dwordx4 v[96:99], v[102:103], off offset:3072
	v_lshl_or_b32 v1, s5, 13, v134
	s_movk_i32 s5, 0x3000
	v_addc_co_u32_e32 v107, vcc, 0, v3, vcc
	v_add_co_u32_e32 v108, vcc, s5, v2
	s_mov_b32 s8, 0x14000
	s_nop 0
	v_addc_co_u32_e32 v109, vcc, 0, v3, vcc
	s_ashr_i32 s5, s4, 31
	s_lshl_b32 s10, s0, 13
	s_lshl_b64 s[0:1], s[4:5], 14
	v_add_co_u32_e32 v100, vcc, s8, v2
	s_mov_b32 s9, 0x15000
	s_add_u32 s0, s2, s0
	v_addc_co_u32_e32 v101, vcc, 0, v3, vcc
	s_addc_u32 s1, s3, s1
	s_and_b32 s2, s10, 0x6000
	v_add_co_u32_e32 v102, vcc, s9, v2
	s_movk_i32 s3, 0x5000
	s_nop 0
	v_addc_co_u32_e32 v103, vcc, 0, v3, vcc
	s_waitcnt vmcnt(23)
	ds_write_b128 v1, v[4:7]
	s_waitcnt vmcnt(22)
	ds_write_b128 v1, v[8:11] offset:1024
	s_waitcnt vmcnt(21)
	ds_write_b128 v1, v[12:15] offset:2048
	s_waitcnt vmcnt(20)
	ds_write_b128 v1, v[16:19] offset:3072
	s_waitcnt vmcnt(19)
	ds_write_b128 v1, v[20:23] offset:4096
	s_waitcnt vmcnt(18)
	ds_write_b128 v1, v[24:27] offset:5120
	s_waitcnt vmcnt(17)
	ds_write_b128 v1, v[28:31] offset:6144
	s_waitcnt vmcnt(16)
	ds_write_b128 v1, v[32:35] offset:7168
	s_waitcnt lgkmcnt(0)
	s_barrier
	global_load_dwordx4 v[4:7], v[106:107], off offset:-4096
	global_load_dwordx4 v[8:11], v[108:109], off offset:1024
	global_load_dwordx4 v[12:15], v[108:109], off offset:2048
	global_load_dwordx4 v[16:19], v[108:109], off offset:3072
	global_load_dwordx4 v[20:23], v[104:105], off
	global_load_dwordx4 v[24:27], v[104:105], off offset:1024
	global_load_dwordx4 v[28:31], v[104:105], off offset:2048
	global_load_dwordx4 v[32:35], v[104:105], off offset:3072
	v_or_b32_e32 v1, s2, v134
	s_waitcnt vmcnt(23)
	ds_write_b128 v1, v[36:39] offset:16384
	s_waitcnt vmcnt(22)
	ds_write_b128 v1, v[40:43] offset:17408
	s_waitcnt vmcnt(21)
	ds_write_b128 v1, v[44:47] offset:18432
	s_waitcnt vmcnt(20)
	ds_write_b128 v1, v[48:51] offset:19456
	s_waitcnt vmcnt(19)
	ds_write_b128 v1, v[52:55] offset:20480
	s_waitcnt vmcnt(18)
	ds_write_b128 v1, v[56:59] offset:21504
	s_waitcnt vmcnt(17)
	ds_write_b128 v1, v[60:63] offset:22528
	s_waitcnt vmcnt(16)
	ds_write_b128 v1, v[64:67] offset:23552
	s_waitcnt lgkmcnt(0)
	s_barrier
	global_load_dwordx4 v[36:39], v[106:107], off
	global_load_dwordx4 v[40:43], v[106:107], off offset:1024
	global_load_dwordx4 v[44:47], v[106:107], off offset:2048
	global_load_dwordx4 v[48:51], v[106:107], off offset:3072
	global_load_dwordx4 v[52:55], v[102:103], off offset:-4096
	global_load_dwordx4 v[56:59], v[100:101], off offset:1024
	global_load_dwordx4 v[60:63], v[100:101], off offset:2048
	global_load_dwordx4 v[64:67], v[100:101], off offset:3072
	s_movk_i32 s2, 0x6000
	v_add_co_u32_e32 v100, vcc, s2, v2
	s_waitcnt vmcnt(23)
	ds_write_b128 v1, v[68:71]
	s_waitcnt vmcnt(22)
	ds_write_b128 v1, v[72:75] offset:1024
	s_waitcnt vmcnt(21)
	ds_write_b128 v1, v[76:79] offset:2048
	s_waitcnt vmcnt(20)
	ds_write_b128 v1, v[80:83] offset:3072
	s_waitcnt vmcnt(19)
	ds_write_b128 v1, v[84:87] offset:4096
	s_waitcnt vmcnt(18)
	ds_write_b128 v1, v[88:91] offset:5120
	s_waitcnt vmcnt(17)
	ds_write_b128 v1, v[92:95] offset:6144
	s_waitcnt vmcnt(16)
	ds_write_b128 v1, v[96:99] offset:7168
	v_addc_co_u32_e32 v101, vcc, 0, v3, vcc
	v_add_co_u32_e32 v104, vcc, s3, v2
	s_waitcnt lgkmcnt(0)
	s_nop 0
	v_addc_co_u32_e32 v105, vcc, 0, v3, vcc
	s_barrier
	global_load_dwordx4 v[68:71], v[104:105], off offset:1024
	global_load_dwordx4 v[72:75], v[104:105], off offset:2048
	global_load_dwordx4 v[76:79], v[104:105], off offset:3072
	global_load_dwordx4 v[80:83], v[102:103], off
	global_load_dwordx4 v[84:87], v[102:103], off offset:1024
	global_load_dwordx4 v[88:91], v[102:103], off offset:2048
	global_load_dwordx4 v[92:95], v[100:101], off offset:-4096
	global_load_dwordx4 v[96:99], v[102:103], off offset:3072
	s_mov_b32 s2, 0x16000
	v_add_co_u32_e32 v102, vcc, s2, v2
	s_mov_b32 s3, 0x17000
	s_nop 0
	v_addc_co_u32_e32 v103, vcc, 0, v3, vcc
	v_add_co_u32_e32 v104, vcc, s3, v2
	s_mov_b32 s3, 0x8000
	s_nop 0
	v_addc_co_u32_e32 v105, vcc, 0, v3, vcc
	s_movk_i32 s2, 0x7000
	v_lshlrev_b32_e32 v134, 4, v0
	s_waitcnt vmcnt(23)
	ds_write_b128 v1, v[4:7] offset:16384
	s_waitcnt vmcnt(22)
	ds_write_b128 v1, v[8:11] offset:17408
	s_waitcnt vmcnt(21)
	ds_write_b128 v1, v[12:15] offset:18432
	s_waitcnt vmcnt(20)
	ds_write_b128 v1, v[16:19] offset:19456
	s_waitcnt vmcnt(19)
	ds_write_b128 v1, v[20:23] offset:20480
	s_waitcnt vmcnt(18)
	ds_write_b128 v1, v[24:27] offset:21504
	s_waitcnt vmcnt(17)
	ds_write_b128 v1, v[28:31] offset:22528
	s_waitcnt vmcnt(16)
	ds_write_b128 v1, v[32:35] offset:23552
	s_waitcnt lgkmcnt(0)
	s_barrier
	global_load_dwordx4 v[4:7], v[100:101], off
	global_load_dwordx4 v[8:11], v[100:101], off offset:1024
	global_load_dwordx4 v[12:15], v[100:101], off offset:2048
	global_load_dwordx4 v[16:19], v[100:101], off offset:3072
	global_load_dwordx4 v[20:23], v[104:105], off offset:-4096
	global_load_dwordx4 v[24:27], v[102:103], off offset:1024
	global_load_dwordx4 v[28:31], v[102:103], off offset:2048
	global_load_dwordx4 v[32:35], v[102:103], off offset:3072
	v_add_co_u32_e32 v100, vcc, s3, v2
	s_waitcnt vmcnt(23)
	ds_write_b128 v1, v[36:39]
	s_waitcnt vmcnt(22)
	ds_write_b128 v1, v[40:43] offset:1024
	s_waitcnt vmcnt(21)
	ds_write_b128 v1, v[44:47] offset:2048
	v_addc_co_u32_e32 v101, vcc, 0, v3, vcc
	v_add_co_u32_e32 v102, vcc, s2, v2
	s_waitcnt vmcnt(20)
	ds_write_b128 v1, v[48:51] offset:3072
	v_addc_co_u32_e32 v103, vcc, 0, v3, vcc
	s_waitcnt vmcnt(19)
	ds_write_b128 v1, v[52:55] offset:4096
	s_waitcnt vmcnt(18)
	ds_write_b128 v1, v[56:59] offset:5120
	s_waitcnt vmcnt(17)
	ds_write_b128 v1, v[60:63] offset:6144
	s_waitcnt vmcnt(16)
	ds_write_b128 v1, v[64:67] offset:7168
	s_waitcnt lgkmcnt(0)
	s_barrier
	global_load_dwordx4 v[36:39], v[100:101], off offset:-4096
	global_load_dwordx4 v[40:43], v[102:103], off offset:1024
	global_load_dwordx4 v[44:47], v[102:103], off offset:2048
	global_load_dwordx4 v[48:51], v[102:103], off offset:3072
	global_load_dwordx4 v[52:55], v[104:105], off
	global_load_dwordx4 v[56:59], v[104:105], off offset:1024
	global_load_dwordx4 v[60:63], v[104:105], off offset:2048
	global_load_dwordx4 v[64:67], v[104:105], off offset:3072
	s_mov_b32 s2, 0x18000
	v_add_co_u32_e32 v102, vcc, s2, v2
	s_mov_b32 s3, 0x19000
	s_nop 0
	v_addc_co_u32_e32 v103, vcc, 0, v3, vcc
	v_add_co_u32_e32 v104, vcc, s3, v2
	s_waitcnt vmcnt(17)
	ds_write_b128 v1, v[92:95] offset:16384
	ds_write_b128 v1, v[68:71] offset:17408
	ds_write_b128 v1, v[72:75] offset:18432
	ds_write_b128 v1, v[76:79] offset:19456
	ds_write_b128 v1, v[80:83] offset:20480
	ds_write_b128 v1, v[84:87] offset:21504
	ds_write_b128 v1, v[88:91] offset:22528
	s_waitcnt vmcnt(16)
	ds_write_b128 v1, v[96:99] offset:23552
	v_addc_co_u32_e32 v105, vcc, 0, v3, vcc
	s_waitcnt lgkmcnt(0)
	s_barrier
	global_load_dwordx4 v[68:71], v[100:101], off
	global_load_dwordx4 v[72:75], v[100:101], off offset:1024
	global_load_dwordx4 v[76:79], v[100:101], off offset:2048
	global_load_dwordx4 v[80:83], v[100:101], off offset:3072
	global_load_dwordx4 v[84:87], v[104:105], off offset:-4096
	global_load_dwordx4 v[88:91], v[102:103], off offset:1024
	global_load_dwordx4 v[92:95], v[102:103], off offset:2048
	s_mov_b32 s3, 0xa000
	v_add_co_u32_e32 v100, vcc, s3, v2
	s_mov_b32 s2, 0x9000
	s_nop 0
	v_addc_co_u32_e32 v101, vcc, 0, v3, vcc
	s_mov_b32 s3, 0xc000
	s_waitcnt vmcnt(22)
	ds_write_b128 v1, v[4:7]
	s_waitcnt vmcnt(21)
	ds_write_b128 v1, v[8:11] offset:1024
	s_waitcnt vmcnt(20)
	ds_write_b128 v1, v[12:15] offset:2048
	global_load_dwordx4 v[4:7], v[102:103], off offset:3072
	s_waitcnt vmcnt(20)
	ds_write_b128 v1, v[16:19] offset:3072
	s_waitcnt vmcnt(19)
	ds_write_b128 v1, v[20:23] offset:4096
	s_waitcnt vmcnt(18)
	ds_write_b128 v1, v[24:27] offset:5120
	s_waitcnt vmcnt(17)
	ds_write_b128 v1, v[28:31] offset:6144
	s_waitcnt vmcnt(16)
	ds_write_b128 v1, v[32:35] offset:7168
	s_waitcnt lgkmcnt(0)
	s_barrier
	global_load_dwordx4 v[8:11], v[100:101], off offset:-4096
	v_add_co_u32_e32 v102, vcc, s2, v2
	s_mov_b32 s2, 0x1a000
	s_nop 0
	v_addc_co_u32_e32 v103, vcc, 0, v3, vcc
	global_load_dwordx4 v[12:15], v[102:103], off offset:1024
	global_load_dwordx4 v[16:19], v[102:103], off offset:2048
	global_load_dwordx4 v[20:23], v[102:103], off offset:3072
	global_load_dwordx4 v[24:27], v[104:105], off
	global_load_dwordx4 v[28:31], v[104:105], off offset:1024
	global_load_dwordx4 v[32:35], v[104:105], off offset:2048
	global_load_dwordx4 v[96:99], v[104:105], off offset:3072
	v_add_co_u32_e32 v102, vcc, s2, v2
	s_mov_b32 s2, 0x1b000
	s_nop 0
	v_addc_co_u32_e32 v103, vcc, 0, v3, vcc
	s_waitcnt vmcnt(23)
	ds_write_b128 v1, v[36:39] offset:16384
	s_waitcnt vmcnt(22)
	ds_write_b128 v1, v[40:43] offset:17408
	s_waitcnt vmcnt(21)
	ds_write_b128 v1, v[44:47] offset:18432
	s_waitcnt vmcnt(20)
	ds_write_b128 v1, v[48:51] offset:19456
	s_waitcnt vmcnt(19)
	ds_write_b128 v1, v[52:55] offset:20480
	s_waitcnt vmcnt(18)
	ds_write_b128 v1, v[56:59] offset:21504
	s_waitcnt vmcnt(17)
	ds_write_b128 v1, v[60:63] offset:22528
	s_waitcnt vmcnt(16)
	ds_write_b128 v1, v[64:67] offset:23552
	s_waitcnt lgkmcnt(0)
	s_barrier
	global_load_dwordx4 v[36:39], v[100:101], off
	global_load_dwordx4 v[40:43], v[100:101], off offset:1024
	global_load_dwordx4 v[44:47], v[100:101], off offset:2048
	v_add_co_u32_e32 v104, vcc, s2, v2
	s_mov_b32 s2, 0xb000
	s_nop 0
	v_addc_co_u32_e32 v105, vcc, 0, v3, vcc
	global_load_dwordx4 v[48:51], v[100:101], off offset:3072
	global_load_dwordx4 v[52:55], v[104:105], off offset:-4096
	global_load_dwordx4 v[56:59], v[102:103], off offset:1024
	global_load_dwordx4 v[60:63], v[102:103], off offset:2048
	global_load_dwordx4 v[64:67], v[102:103], off offset:3072
	s_waitcnt vmcnt(23)
	ds_write_b128 v1, v[68:71]
	s_waitcnt vmcnt(22)
	ds_write_b128 v1, v[72:75] offset:1024
	s_waitcnt vmcnt(21)
	ds_write_b128 v1, v[76:79] offset:2048
	s_waitcnt vmcnt(20)
	ds_write_b128 v1, v[80:83] offset:3072
	s_waitcnt vmcnt(19)
	ds_write_b128 v1, v[84:87] offset:4096
	s_waitcnt vmcnt(18)
	ds_write_b128 v1, v[88:91] offset:5120
	s_waitcnt vmcnt(17)
	ds_write_b128 v1, v[92:95] offset:6144
	s_waitcnt vmcnt(16)
	ds_write_b128 v1, v[4:7] offset:7168
	v_add_co_u32_e32 v84, vcc, s3, v2
	s_waitcnt lgkmcnt(0)
	s_nop 0
	v_addc_co_u32_e32 v85, vcc, 0, v3, vcc
	v_add_co_u32_e32 v80, vcc, s2, v2
	s_barrier
	s_nop 0
	v_addc_co_u32_e32 v81, vcc, 0, v3, vcc
	global_load_dwordx4 v[4:7], v[84:85], off offset:-4096
	global_load_dwordx4 v[68:71], v[80:81], off offset:1024
	global_load_dwordx4 v[72:75], v[80:81], off offset:2048
	s_waitcnt vmcnt(18)
	ds_write_b128 v1, v[8:11] offset:16384
	global_load_dwordx4 v[8:11], v[80:81], off offset:3072
	global_load_dwordx4 v[76:79], v[104:105], off
	s_waitcnt vmcnt(19)
	ds_write_b128 v1, v[12:15] offset:17408
	s_waitcnt vmcnt(18)
	ds_write_b128 v1, v[16:19] offset:18432
	s_mov_b32 s2, 0x1c000
	global_load_dwordx4 v[12:15], v[104:105], off offset:1024
	global_load_dwordx4 v[16:19], v[104:105], off offset:2048
	global_load_dwordx4 v[80:83], v[104:105], off offset:3072
	v_add_co_u32_e32 v88, vcc, s2, v2
	s_mov_b32 s2, 0x1d000
	s_nop 0
	v_addc_co_u32_e32 v89, vcc, 0, v3, vcc
	v_add_co_u32_e32 v100, vcc, s2, v2
	s_mov_b32 s3, 0xe000
	s_nop 0
	v_addc_co_u32_e32 v101, vcc, 0, v3, vcc
	s_waitcnt vmcnt(20)
	ds_write_b128 v1, v[20:23] offset:19456
	s_waitcnt vmcnt(19)
	ds_write_b128 v1, v[24:27] offset:20480
	s_waitcnt vmcnt(18)
	ds_write_b128 v1, v[28:31] offset:21504
	s_waitcnt vmcnt(17)
	ds_write_b128 v1, v[32:35] offset:22528
	s_waitcnt vmcnt(16)
	ds_write_b128 v1, v[96:99] offset:23552
	s_waitcnt lgkmcnt(0)
	s_barrier
	global_load_dwordx4 v[20:23], v[84:85], off
	global_load_dwordx4 v[24:27], v[84:85], off offset:1024
	global_load_dwordx4 v[28:31], v[84:85], off offset:2048
	s_waitcnt vmcnt(18)
	ds_write_b128 v1, v[36:39]
	v_add_co_u32_e32 v102, vcc, s3, v2
	global_load_dwordx4 v[32:35], v[84:85], off offset:3072
	global_load_dwordx4 v[36:39], v[100:101], off offset:-4096
	s_waitcnt vmcnt(19)
	ds_write_b128 v1, v[40:43] offset:1024
	s_waitcnt vmcnt(18)
	ds_write_b128 v1, v[44:47] offset:2048
	s_mov_b32 s2, 0xd000
	v_addc_co_u32_e32 v103, vcc, 0, v3, vcc
	global_load_dwordx4 v[40:43], v[88:89], off offset:1024
	global_load_dwordx4 v[44:47], v[88:89], off offset:2048
	global_load_dwordx4 v[84:87], v[88:89], off offset:3072
	s_waitcnt vmcnt(20)
	ds_write_b128 v1, v[48:51] offset:3072
	s_waitcnt vmcnt(19)
	ds_write_b128 v1, v[52:55] offset:4096
	s_waitcnt vmcnt(18)
	ds_write_b128 v1, v[56:59] offset:5120
	s_waitcnt vmcnt(17)
	ds_write_b128 v1, v[60:63] offset:6144
	s_waitcnt vmcnt(16)
	ds_write_b128 v1, v[64:67] offset:7168
	s_waitcnt lgkmcnt(0)
	s_barrier
	global_load_dwordx4 v[48:51], v[102:103], off offset:-4096
	v_add_co_u32_e32 v104, vcc, s2, v2
	s_mov_b32 s2, 0x1e000
	s_nop 0
	v_addc_co_u32_e32 v105, vcc, 0, v3, vcc
	global_load_dwordx4 v[52:55], v[104:105], off offset:1024
	global_load_dwordx4 v[56:59], v[104:105], off offset:2048
	global_load_dwordx4 v[60:63], v[104:105], off offset:3072
	global_load_dwordx4 v[64:67], v[100:101], off
	global_load_dwordx4 v[88:91], v[100:101], off offset:1024
	global_load_dwordx4 v[92:95], v[100:101], off offset:2048
	global_load_dwordx4 v[96:99], v[100:101], off offset:3072
	v_add_u32_e32 v100, 0xffffff00, v0
	v_ashrrev_i32_e32 v101, 31, v100
	v_lshlrev_b32_e32 v0, 4, v100
	s_waitcnt vmcnt(23)
	ds_write_b128 v1, v[4:7] offset:16384
	s_waitcnt vmcnt(22)
	ds_write_b128 v1, v[68:71] offset:17408
	s_waitcnt vmcnt(21)
	ds_write_b128 v1, v[72:75] offset:18432
	s_waitcnt vmcnt(20)
	ds_write_b128 v1, v[8:11] offset:19456
	s_waitcnt vmcnt(19)
	ds_write_b128 v1, v[76:79] offset:20480
	s_waitcnt vmcnt(18)
	ds_write_b128 v1, v[12:15] offset:21504
	s_waitcnt vmcnt(17)
	ds_write_b128 v1, v[16:19] offset:22528
	s_waitcnt vmcnt(16)
	ds_write_b128 v1, v[80:83] offset:23552
	v_add_co_u32_e32 v68, vcc, s2, v2
	s_mov_b32 s2, 0x1f000
	s_nop 0
	v_addc_co_u32_e32 v69, vcc, 0, v3, vcc
	v_add_co_u32_e32 v76, vcc, s2, v2
	s_waitcnt lgkmcnt(0)
	s_barrier
	global_load_dwordx4 v[4:7], v[102:103], off offset:1024
	global_load_dwordx4 v[8:11], v[102:103], off offset:2048
	v_addc_co_u32_e32 v77, vcc, 0, v3, vcc
	s_waitcnt vmcnt(17)
	ds_write_b128 v1, v[20:23]
	s_mov_b32 s2, 0xf000
	global_load_dwordx4 v[12:15], v[102:103], off offset:3072
	global_load_dwordx4 v[16:19], v[76:77], off offset:-4096
	s_waitcnt vmcnt(18)
	ds_write_b128 v1, v[24:27] offset:1024
	s_waitcnt vmcnt(17)
	ds_write_b128 v1, v[28:31] offset:2048
	v_add_co_u32_e32 v2, vcc, s2, v2
	global_load_dwordx4 v[20:23], v[68:69], off offset:1024
	global_load_dwordx4 v[24:27], v[68:69], off offset:2048
	s_waitcnt vmcnt(18)
	ds_write_b128 v1, v[32:35] offset:3072
	v_addc_co_u32_e32 v3, vcc, 0, v3, vcc
	global_load_dwordx4 v[28:31], v[102:103], off
	global_load_dwordx4 v[32:35], v[68:69], off offset:3072
	s_waitcnt vmcnt(19)
	ds_write_b128 v1, v[36:39] offset:4096
	s_waitcnt vmcnt(18)
	ds_write_b128 v1, v[40:43] offset:5120
	s_waitcnt vmcnt(17)
	ds_write_b128 v1, v[44:47] offset:6144
	s_waitcnt vmcnt(16)
	ds_write_b128 v1, v[84:87] offset:7168
	s_waitcnt lgkmcnt(0)
	s_barrier
	global_load_dwordx4 v[36:39], v[2:3], off
	global_load_dwordx4 v[40:43], v[2:3], off offset:1024
	global_load_dwordx4 v[44:47], v[2:3], off offset:2048
	global_load_dwordx4 v[68:71], v[2:3], off offset:3072
	s_waitcnt vmcnt(19)
	ds_write_b128 v1, v[48:51] offset:16384
	global_load_dwordx4 v[48:51], v[76:77], off
	global_load_dwordx4 v[72:75], v[76:77], off offset:1024
	s_waitcnt vmcnt(20)
	ds_write_b128 v1, v[52:55] offset:17408
	s_waitcnt vmcnt(19)
	ds_write_b128 v1, v[56:59] offset:18432
	v_lshl_add_u64 v[2:3], v[100:101], 4, s[0:1]
	global_load_dwordx4 v[52:55], v[76:77], off offset:2048
	global_load_dwordx4 v[56:59], v[76:77], off offset:3072
	s_waitcnt vmcnt(20)
	ds_write_b128 v1, v[60:63] offset:19456
	s_waitcnt vmcnt(19)
	ds_write_b128 v1, v[64:67] offset:20480
	s_waitcnt vmcnt(18)
	ds_write_b128 v1, v[88:91] offset:21504
	s_waitcnt vmcnt(17)
	ds_write_b128 v1, v[92:95] offset:22528
	s_waitcnt vmcnt(16)
	ds_write_b128 v1, v[96:99] offset:23552
	s_waitcnt lgkmcnt(0)
	s_barrier
	global_load_dwordx4 v[60:63], v[2:3], off
	v_lshl_add_u64 v[2:3], s[0:1], 0, v[134:135]
	v_add_co_u32_e32 v102, vcc, s6, v2
	global_load_dwordx4 v[64:67], v134, s[0:1] offset:-2048
	global_load_dwordx4 v[76:79], v134, s[0:1]
	v_addc_co_u32_e32 v103, vcc, 0, v3, vcc
	v_add_co_u32_e32 v2, vcc, s7, v2
	s_nop 1
	v_addc_co_u32_e32 v3, vcc, 0, v3, vcc
	global_load_dwordx4 v[80:83], v134, s[0:1] offset:2048
	global_load_dwordx4 v[84:87], v[2:3], off offset:-4096
	global_load_dwordx4 v[88:91], v[102:103], off offset:2048
	global_load_dwordx4 v[92:95], v[2:3], off
	global_load_dwordx4 v[96:99], v[2:3], off offset:2048
	s_waitcnt vmcnt(17)
	ds_write_b128 v1, v[28:31]
	ds_write_b128 v1, v[4:7] offset:1024
	ds_write_b128 v1, v[8:11] offset:2048
	ds_write_b128 v1, v[12:15] offset:3072
	ds_write_b128 v1, v[16:19] offset:4096
	ds_write_b128 v1, v[20:23] offset:5120
	ds_write_b128 v1, v[24:27] offset:6144
	s_waitcnt vmcnt(16)
	ds_write_b128 v1, v[32:35] offset:7168
	s_waitcnt lgkmcnt(0)
	s_barrier
	s_waitcnt vmcnt(15)
	ds_write_b128 v1, v[36:39] offset:16384
	s_waitcnt vmcnt(14)
	ds_write_b128 v1, v[40:43] offset:17408
	s_waitcnt vmcnt(13)
	ds_write_b128 v1, v[44:47] offset:18432
	s_waitcnt vmcnt(12)
	ds_write_b128 v1, v[68:71] offset:19456
	s_waitcnt vmcnt(11)
	ds_write_b128 v1, v[48:51] offset:20480
	s_waitcnt vmcnt(10)
	ds_write_b128 v1, v[72:75] offset:21504
	s_waitcnt vmcnt(9)
	ds_write_b128 v1, v[52:55] offset:22528
	s_waitcnt vmcnt(8)
	ds_write_b128 v1, v[56:59] offset:23552
	s_waitcnt lgkmcnt(0)
	s_barrier
	s_waitcnt vmcnt(7)
	ds_write_b128 v0, v[60:63] offset:33792
	s_waitcnt vmcnt(6)
	ds_write_b128 v0, v[64:67] offset:35840
	s_waitcnt vmcnt(5)
	ds_write_b128 v0, v[76:79] offset:37888
	s_waitcnt vmcnt(4)
	ds_write_b128 v0, v[80:83] offset:39936
	s_waitcnt vmcnt(3)
	ds_write_b128 v0, v[84:87] offset:41984
	s_waitcnt vmcnt(2)
	ds_write_b128 v0, v[88:91] offset:44032
	s_waitcnt vmcnt(1)
	ds_write_b128 v0, v[92:95] offset:46080
	s_waitcnt vmcnt(0)
	ds_write_b128 v0, v[96:99] offset:48128
	s_waitcnt lgkmcnt(0)
	s_barrier
	s_endpgm
	s_nop 0
	s_nop 0
	s_nop 0
	s_nop 0
	s_nop 0
	s_nop 0
	s_nop 0
	s_nop 0
	s_nop 0
	s_nop 0
	s_nop 0
	s_nop 0
	s_nop 0
	s_nop 0
	s_nop 0
	s_nop 0
	s_nop 0
	s_nop 0
	s_nop 0
	s_nop 0
	s_nop 0
	s_nop 0
	s_nop 0
	s_nop 0
	s_nop 0
	s_nop 0
	s_nop 0
	s_nop 0
	s_nop 0
	s_nop 0
	s_nop 0
	s_nop 0
	s_nop 0
	s_nop 0
	s_nop 0
	s_nop 0
	s_nop 0
	s_nop 0
	s_nop 0
	s_nop 0
	s_nop 0
	s_nop 0
	s_nop 0
	s_nop 0
	s_nop 0
	s_nop 0
	s_nop 0
	s_nop 0
	s_nop 0
	s_nop 0
	s_nop 0
	s_nop 0
	s_nop 0
	s_nop 0
	s_nop 0
	s_nop 0
	s_nop 0
	s_nop 0
	s_nop 0
	s_nop 0
	s_endpgm
